# previous + dead lgkmcnt waits and mid-segment s_setprio 0/1 flips removed from GEMM MFMA segments
# speedup vs baseline: 1.0067x; 1.0012x over previous
.LBB0_319:
	s_and_b64 s[40:41], s[38:39], exec
	s_cselect_b32 s44, 0, s36
	s_add_u32 s40, s34, s36
	s_addc_u32 s41, s35, s37
	s_waitcnt vmcnt(8)
	s_and_b64 s[38:39], s[38:39], exec
	s_waitcnt lgkmcnt(0)
	s_cselect_b32 s38, s29, s40
	s_cselect_b32 s39, s20, s41
	s_add_u32 s42, s38, 0x80
	s_addc_u32 s43, s39, 0
	s_barrier
	s_setprio 1
	v_mfma_f32_16x16x32_bf16 v[126:129], v[146:149], v[186:189], v[126:129]
	v_mfma_f32_16x16x32_bf16 v[122:125], v[154:157], v[186:189], v[122:125]
	v_mfma_f32_16x16x32_bf16 v[118:121], v[146:149], v[178:181], v[118:121]
	v_mfma_f32_16x16x32_bf16 v[110:113], v[154:157], v[178:181], v[110:113]
	v_mfma_f32_16x16x32_bf16 v[102:105], v[146:149], v[170:173], v[102:105]
	v_mfma_f32_16x16x32_bf16 v[94:97], v[154:157], v[170:173], v[94:97]
	v_mfma_f32_16x16x32_bf16 v[86:89], v[146:149], v[162:165], v[86:89]
	v_mfma_f32_16x16x32_bf16 v[78:81], v[154:157], v[162:165], v[78:81]
	v_mfma_f32_16x16x32_bf16 v[126:129], v[150:153], v[190:193], v[126:129]
	v_mfma_f32_16x16x32_bf16 v[122:125], v[158:161], v[190:193], v[122:125]
	v_mfma_f32_16x16x32_bf16 v[118:121], v[150:153], v[182:185], v[118:121]
	v_mfma_f32_16x16x32_bf16 v[110:113], v[158:161], v[182:185], v[110:113]
	v_mfma_f32_16x16x32_bf16 v[102:105], v[150:153], v[174:177], v[102:105]
	v_mfma_f32_16x16x32_bf16 v[94:97], v[158:161], v[174:177], v[94:97]
	v_mfma_f32_16x16x32_bf16 v[86:89], v[150:153], v[166:169], v[86:89]
	v_mfma_f32_16x16x32_bf16 v[78:81], v[158:161], v[166:169], v[78:81]
	v_mfma_f32_16x16x32_bf16 v[114:117], v[130:133], v[186:189], v[114:117]
	v_mfma_f32_16x16x32_bf16 v[106:109], v[138:141], v[186:189], v[106:109]
	v_mfma_f32_16x16x32_bf16 v[98:101], v[130:133], v[178:181], v[98:101]
	v_mfma_f32_16x16x32_bf16 v[90:93], v[138:141], v[178:181], v[90:93]
	v_mfma_f32_16x16x32_bf16 v[82:85], v[130:133], v[170:173], v[82:85]
	v_mfma_f32_16x16x32_bf16 v[74:77], v[138:141], v[170:173], v[74:77]
	v_mfma_f32_16x16x32_bf16 v[70:73], v[130:133], v[162:165], v[70:73]
	v_mfma_f32_16x16x32_bf16 v[66:69], v[138:141], v[162:165], v[66:69]
	v_mfma_f32_16x16x32_bf16 v[114:117], v[134:137], v[190:193], v[114:117]
	v_mfma_f32_16x16x32_bf16 v[106:109], v[142:145], v[190:193], v[106:109]
	v_mfma_f32_16x16x32_bf16 v[98:101], v[134:137], v[182:185], v[98:101]
	v_mfma_f32_16x16x32_bf16 v[90:93], v[142:145], v[182:185], v[90:93]
	v_mfma_f32_16x16x32_bf16 v[82:85], v[134:137], v[174:177], v[82:85]
	v_mfma_f32_16x16x32_bf16 v[74:77], v[142:145], v[174:177], v[74:77]
	v_mfma_f32_16x16x32_bf16 v[70:73], v[134:137], v[166:169], v[70:73]
	v_mfma_f32_16x16x32_bf16 v[66:69], v[142:145], v[166:169], v[66:69]
	s_setprio 0
	s_barrier
	ds_read_b128 v[162:165], v228 offset:16384
	ds_read_b128 v[166:169], v228 offset:17408
	ds_read_b128 v[170:173], v228 offset:18432
	ds_read_b128 v[174:177], v228 offset:19456
	ds_read_b128 v[178:181], v228 offset:20480
	ds_read_b128 v[182:185], v228 offset:21504
	ds_read_b128 v[186:189], v228 offset:22528
	ds_read_b128 v[190:193], v228 offset:23552
	s_mov_b32 m0, s49
	s_nop 0
	global_load_lds_dwordx4 v200, s[38:39]
	s_add_u32 s40, s38, 0x80000
	s_mov_b32 m0, s50
	s_nop 0
	global_load_lds_dwordx4 v201, s[38:39]
	s_addc_u32 s41, s39, 0
	s_mov_b32 m0, s51
	s_nop 0
	global_load_lds_dwordx4 v200, s[40:41]
	s_add_u32 s44, s26, s44
	s_mov_b32 m0, s52
	s_nop 0
	global_load_lds_dwordx4 v201, s[40:41]
	s_addc_u32 s45, s27, 0
	s_mov_b32 m0, s48
	s_nop 0
	global_load_lds_dwordx4 v218, s[44:45]
	s_nop 0
	s_mov_b32 m0, s53
	s_nop 0
	global_load_lds_dwordx4 v220, s[44:45]
	s_waitcnt vmcnt(8)
	s_waitcnt lgkmcnt(0)
	s_barrier
	s_setprio 1
	v_mfma_f32_16x16x32_bf16 v[62:65], v[146:149], v[162:165], v[62:65]
	v_mfma_f32_16x16x32_bf16 v[58:61], v[154:157], v[162:165], v[58:61]
	v_mfma_f32_16x16x32_bf16 v[54:57], v[146:149], v[170:173], v[54:57]
	v_mfma_f32_16x16x32_bf16 v[46:49], v[154:157], v[170:173], v[46:49]
	v_mfma_f32_16x16x32_bf16 v[38:41], v[146:149], v[178:181], v[38:41]
	v_mfma_f32_16x16x32_bf16 v[30:33], v[154:157], v[178:181], v[30:33]
	v_mfma_f32_16x16x32_bf16 v[22:25], v[146:149], v[186:189], v[22:25]
	v_mfma_f32_16x16x32_bf16 v[14:17], v[154:157], v[186:189], v[14:17]
	v_mfma_f32_16x16x32_bf16 v[62:65], v[150:153], v[166:169], v[62:65]
	v_mfma_f32_16x16x32_bf16 v[58:61], v[158:161], v[166:169], v[58:61]
	v_mfma_f32_16x16x32_bf16 v[54:57], v[150:153], v[174:177], v[54:57]
	v_mfma_f32_16x16x32_bf16 v[46:49], v[158:161], v[174:177], v[46:49]
	v_mfma_f32_16x16x32_bf16 v[38:41], v[150:153], v[182:185], v[38:41]
	v_mfma_f32_16x16x32_bf16 v[30:33], v[158:161], v[182:185], v[30:33]
	v_mfma_f32_16x16x32_bf16 v[22:25], v[150:153], v[190:193], v[22:25]
	v_mfma_f32_16x16x32_bf16 v[14:17], v[158:161], v[190:193], v[14:17]
	v_mfma_f32_16x16x32_bf16 v[50:53], v[130:133], v[162:165], v[50:53]
	v_mfma_f32_16x16x32_bf16 v[42:45], v[138:141], v[162:165], v[42:45]
	v_mfma_f32_16x16x32_bf16 v[34:37], v[130:133], v[170:173], v[34:37]
	v_mfma_f32_16x16x32_bf16 v[26:29], v[138:141], v[170:173], v[26:29]
	v_mfma_f32_16x16x32_bf16 v[18:21], v[130:133], v[178:181], v[18:21]
	v_mfma_f32_16x16x32_bf16 v[10:13], v[138:141], v[178:181], v[10:13]
	v_mfma_f32_16x16x32_bf16 v[6:9], v[130:133], v[186:189], v[6:9]
	v_mfma_f32_16x16x32_bf16 v[2:5], v[138:141], v[186:189], v[2:5]
	v_mfma_f32_16x16x32_bf16 v[50:53], v[134:137], v[166:169], v[50:53]
	v_mfma_f32_16x16x32_bf16 v[42:45], v[142:145], v[166:169], v[42:45]
	v_mfma_f32_16x16x32_bf16 v[34:37], v[134:137], v[174:177], v[34:37]
	v_mfma_f32_16x16x32_bf16 v[26:29], v[142:145], v[174:177], v[26:29]
	v_mfma_f32_16x16x32_bf16 v[18:21], v[134:137], v[182:185], v[18:21]
	v_mfma_f32_16x16x32_bf16 v[10:13], v[142:145], v[182:185], v[10:13]
	v_mfma_f32_16x16x32_bf16 v[6:9], v[134:137], v[190:193], v[6:9]
	v_mfma_f32_16x16x32_bf16 v[2:5], v[142:145], v[190:193], v[2:5]
	s_setprio 0
	s_barrier
	v_add_u32_e32 v142, 0x18000, v225
	v_add_u32_e32 v158, 0x1c000, v225
	ds_read_b128 v[130:133], v142
	ds_read_b128 v[134:137], v142 offset:1024
	ds_read_b128 v[138:141], v142 offset:2048
	ds_read_b128 v[142:145], v142 offset:3072
	ds_read_b128 v[146:149], v158
	ds_read_b128 v[150:153], v158 offset:1024
	ds_read_b128 v[154:157], v158 offset:2048
	ds_read_b128 v[158:161], v158 offset:3072
	ds_read_b128 v[162:165], v228 offset:32768
	ds_read_b128 v[166:169], v228 offset:33792
	ds_read_b128 v[170:173], v228 offset:34816
	ds_read_b128 v[174:177], v228 offset:35840
	ds_read_b128 v[178:181], v228 offset:36864
	ds_read_b128 v[182:185], v228 offset:37888
	ds_read_b128 v[186:189], v228 offset:38912
	ds_read_b128 v[190:193], v228 offset:39936
	s_mov_b32 m0, s54
	s_nop 0
	global_load_lds_dwordx4 v219, s[44:45]
	s_nop 0
	s_mov_b32 m0, s55
	s_nop 0
	global_load_lds_dwordx4 v221, s[44:45]
	s_waitcnt vmcnt(8)
	s_waitcnt lgkmcnt(0)
	s_barrier
	s_setprio 1
	v_mfma_f32_16x16x32_bf16 v[126:129], v[130:133], v[162:165], v[126:129]
	v_mfma_f32_16x16x32_bf16 v[122:125], v[138:141], v[162:165], v[122:125]
	v_mfma_f32_16x16x32_bf16 v[118:121], v[130:133], v[170:173], v[118:121]
	v_mfma_f32_16x16x32_bf16 v[110:113], v[138:141], v[170:173], v[110:113]
	v_mfma_f32_16x16x32_bf16 v[102:105], v[130:133], v[178:181], v[102:105]
	v_mfma_f32_16x16x32_bf16 v[94:97], v[138:141], v[178:181], v[94:97]
	v_mfma_f32_16x16x32_bf16 v[86:89], v[130:133], v[186:189], v[86:89]
	v_mfma_f32_16x16x32_bf16 v[78:81], v[138:141], v[186:189], v[78:81]
	v_mfma_f32_16x16x32_bf16 v[126:129], v[134:137], v[166:169], v[126:129]
	v_mfma_f32_16x16x32_bf16 v[122:125], v[142:145], v[166:169], v[122:125]
	v_mfma_f32_16x16x32_bf16 v[118:121], v[134:137], v[174:177], v[118:121]
	v_mfma_f32_16x16x32_bf16 v[110:113], v[142:145], v[174:177], v[110:113]
	v_mfma_f32_16x16x32_bf16 v[102:105], v[134:137], v[182:185], v[102:105]
	v_mfma_f32_16x16x32_bf16 v[94:97], v[142:145], v[182:185], v[94:97]
	v_mfma_f32_16x16x32_bf16 v[86:89], v[134:137], v[190:193], v[86:89]
	v_mfma_f32_16x16x32_bf16 v[78:81], v[142:145], v[190:193], v[78:81]
	v_mfma_f32_16x16x32_bf16 v[114:117], v[146:149], v[162:165], v[114:117]
	v_mfma_f32_16x16x32_bf16 v[106:109], v[154:157], v[162:165], v[106:109]
	v_mfma_f32_16x16x32_bf16 v[98:101], v[146:149], v[170:173], v[98:101]
	v_mfma_f32_16x16x32_bf16 v[90:93], v[154:157], v[170:173], v[90:93]
	v_mfma_f32_16x16x32_bf16 v[82:85], v[146:149], v[178:181], v[82:85]
	v_mfma_f32_16x16x32_bf16 v[74:77], v[154:157], v[178:181], v[74:77]
	v_mfma_f32_16x16x32_bf16 v[70:73], v[146:149], v[186:189], v[70:73]
	v_mfma_f32_16x16x32_bf16 v[66:69], v[154:157], v[186:189], v[66:69]
	v_mfma_f32_16x16x32_bf16 v[114:117], v[150:153], v[166:169], v[114:117]
	v_mfma_f32_16x16x32_bf16 v[106:109], v[158:161], v[166:169], v[106:109]
	v_mfma_f32_16x16x32_bf16 v[98:101], v[150:153], v[174:177], v[98:101]
	v_mfma_f32_16x16x32_bf16 v[90:93], v[158:161], v[174:177], v[90:93]
	v_mfma_f32_16x16x32_bf16 v[82:85], v[150:153], v[182:185], v[82:85]
	v_mfma_f32_16x16x32_bf16 v[74:77], v[158:161], v[182:185], v[74:77]
	v_mfma_f32_16x16x32_bf16 v[70:73], v[150:153], v[190:193], v[70:73]
	v_mfma_f32_16x16x32_bf16 v[66:69], v[158:161], v[190:193], v[66:69]
	s_setprio 0
	s_barrier
	ds_read_b128 v[162:165], v228 offset:49152
	ds_read_b128 v[166:169], v228 offset:50176
	ds_read_b128 v[170:173], v228 offset:51200
	ds_read_b128 v[174:177], v228 offset:52224
	ds_read_b128 v[178:181], v228 offset:53248
	ds_read_b128 v[182:185], v228 offset:54272
	ds_read_b128 v[186:189], v228 offset:55296
	ds_read_b128 v[190:193], v228 offset:56320
	s_mov_b32 m0, s56
	s_nop 0
	global_load_lds_dwordx4 v200, s[42:43]
	s_add_u32 s38, s38, 0x80080
	s_mov_b32 m0, s57
	s_nop 0
	global_load_lds_dwordx4 v201, s[42:43]
	s_addc_u32 s39, s39, 0
	s_mov_b32 m0, s60
	s_nop 0
	global_load_lds_dwordx4 v200, s[38:39]
	s_nop 0
	s_mov_b32 m0, s61
	s_nop 0
	global_load_lds_dwordx4 v201, s[38:39]
	s_add_u32 s38, s44, 0x80
	s_addc_u32 s39, s45, 0
	s_mov_b32 m0, s58
	s_nop 0
	global_load_lds_dwordx4 v218, s[38:39]
	s_nop 0
	s_mov_b32 m0, s59
	s_nop 0
	global_load_lds_dwordx4 v220, s[38:39]
	s_waitcnt vmcnt(8)
	s_waitcnt lgkmcnt(0)
	s_barrier
	s_setprio 1
	v_mfma_f32_16x16x32_bf16 v[62:65], v[130:133], v[162:165], v[62:65]
	v_mfma_f32_16x16x32_bf16 v[58:61], v[138:141], v[162:165], v[58:61]
	v_mfma_f32_16x16x32_bf16 v[54:57], v[130:133], v[170:173], v[54:57]
	v_mfma_f32_16x16x32_bf16 v[46:49], v[138:141], v[170:173], v[46:49]
	v_mfma_f32_16x16x32_bf16 v[38:41], v[130:133], v[178:181], v[38:41]
	v_mfma_f32_16x16x32_bf16 v[30:33], v[138:141], v[178:181], v[30:33]
	v_mfma_f32_16x16x32_bf16 v[22:25], v[130:133], v[186:189], v[22:25]
	v_mfma_f32_16x16x32_bf16 v[14:17], v[138:141], v[186:189], v[14:17]
	v_mfma_f32_16x16x32_bf16 v[62:65], v[134:137], v[166:169], v[62:65]
	v_mfma_f32_16x16x32_bf16 v[58:61], v[142:145], v[166:169], v[58:61]
	v_mfma_f32_16x16x32_bf16 v[54:57], v[134:137], v[174:177], v[54:57]
	v_mfma_f32_16x16x32_bf16 v[46:49], v[142:145], v[174:177], v[46:49]
	v_mfma_f32_16x16x32_bf16 v[38:41], v[134:137], v[182:185], v[38:41]
	v_mfma_f32_16x16x32_bf16 v[30:33], v[142:145], v[182:185], v[30:33]
	v_mfma_f32_16x16x32_bf16 v[22:25], v[134:137], v[190:193], v[22:25]
	v_mfma_f32_16x16x32_bf16 v[14:17], v[142:145], v[190:193], v[14:17]
	v_mfma_f32_16x16x32_bf16 v[50:53], v[146:149], v[162:165], v[50:53]
	v_mfma_f32_16x16x32_bf16 v[42:45], v[154:157], v[162:165], v[42:45]
	v_mfma_f32_16x16x32_bf16 v[34:37], v[146:149], v[170:173], v[34:37]
	v_mfma_f32_16x16x32_bf16 v[26:29], v[154:157], v[170:173], v[26:29]
	v_mfma_f32_16x16x32_bf16 v[18:21], v[146:149], v[178:181], v[18:21]
	v_mfma_f32_16x16x32_bf16 v[10:13], v[154:157], v[178:181], v[10:13]
	v_mfma_f32_16x16x32_bf16 v[6:9], v[146:149], v[186:189], v[6:9]
	v_mfma_f32_16x16x32_bf16 v[2:5], v[154:157], v[186:189], v[2:5]
	v_mfma_f32_16x16x32_bf16 v[50:53], v[150:153], v[166:169], v[50:53]
	v_mfma_f32_16x16x32_bf16 v[42:45], v[158:161], v[166:169], v[42:45]
	v_mfma_f32_16x16x32_bf16 v[34:37], v[150:153], v[174:177], v[34:37]
	v_mfma_f32_16x16x32_bf16 v[26:29], v[158:161], v[174:177], v[26:29]
	v_mfma_f32_16x16x32_bf16 v[18:21], v[150:153], v[182:185], v[18:21]
	v_mfma_f32_16x16x32_bf16 v[10:13], v[158:161], v[182:185], v[10:13]
	v_mfma_f32_16x16x32_bf16 v[6:9], v[150:153], v[190:193], v[6:9]
	v_mfma_f32_16x16x32_bf16 v[2:5], v[158:161], v[190:193], v[2:5]
	s_setprio 0
	s_barrier
	s_add_i32 s33, s33, 2
	s_add_u32 s36, s36, 0x100
	s_addc_u32 s37, s37, 0
	s_cmp_gt_u32 s33, 29
	s_cbranch_scc1 .LBB0_324

.LBB0_369:
	s_and_b64 s[30:31], s[28:29], exec
	s_cselect_b32 s59, 0, s26
	s_add_u32 s30, s22, s26
	s_addc_u32 s31, s23, s27
	s_waitcnt vmcnt(8)
	s_and_b64 s[28:29], s[28:29], exec
	s_waitcnt lgkmcnt(0)
	s_cselect_b32 s28, s57, s30
	s_cselect_b32 s29, s21, s31
	s_add_u32 s30, s28, 0x80
	s_addc_u32 s31, s29, 0
	s_barrier
	s_setprio 1
	v_mfma_f32_16x16x32_bf16 v[126:129], v[146:149], v[186:189], v[126:129]
	v_mfma_f32_16x16x32_bf16 v[122:125], v[154:157], v[186:189], v[122:125]
	v_mfma_f32_16x16x32_bf16 v[118:121], v[146:149], v[178:181], v[118:121]
	v_mfma_f32_16x16x32_bf16 v[114:117], v[154:157], v[178:181], v[114:117]
	v_mfma_f32_16x16x32_bf16 v[110:113], v[146:149], v[170:173], v[110:113]
	v_mfma_f32_16x16x32_bf16 v[106:109], v[154:157], v[170:173], v[106:109]
	v_mfma_f32_16x16x32_bf16 v[102:105], v[146:149], v[162:165], v[102:105]
	v_mfma_f32_16x16x32_bf16 v[98:101], v[154:157], v[162:165], v[98:101]
	v_mfma_f32_16x16x32_bf16 v[126:129], v[150:153], v[190:193], v[126:129]
	v_mfma_f32_16x16x32_bf16 v[122:125], v[158:161], v[190:193], v[122:125]
	v_mfma_f32_16x16x32_bf16 v[118:121], v[150:153], v[182:185], v[118:121]
	v_mfma_f32_16x16x32_bf16 v[114:117], v[158:161], v[182:185], v[114:117]
	v_mfma_f32_16x16x32_bf16 v[110:113], v[150:153], v[174:177], v[110:113]
	v_mfma_f32_16x16x32_bf16 v[106:109], v[158:161], v[174:177], v[106:109]
	v_mfma_f32_16x16x32_bf16 v[102:105], v[150:153], v[166:169], v[102:105]
	v_mfma_f32_16x16x32_bf16 v[98:101], v[158:161], v[166:169], v[98:101]
	v_mfma_f32_16x16x32_bf16 v[78:81], v[130:133], v[186:189], v[78:81]
	v_mfma_f32_16x16x32_bf16 v[70:73], v[138:141], v[186:189], v[70:73]
	v_mfma_f32_16x16x32_bf16 v[62:65], v[130:133], v[178:181], v[62:65]
	v_mfma_f32_16x16x32_bf16 v[54:57], v[138:141], v[178:181], v[54:57]
	v_mfma_f32_16x16x32_bf16 v[46:49], v[130:133], v[170:173], v[46:49]
	v_mfma_f32_16x16x32_bf16 v[42:45], v[138:141], v[170:173], v[42:45]
	v_mfma_f32_16x16x32_bf16 v[38:41], v[130:133], v[162:165], v[38:41]
	v_mfma_f32_16x16x32_bf16 v[34:37], v[138:141], v[162:165], v[34:37]
	v_mfma_f32_16x16x32_bf16 v[78:81], v[134:137], v[190:193], v[78:81]
	v_mfma_f32_16x16x32_bf16 v[70:73], v[142:145], v[190:193], v[70:73]
	v_mfma_f32_16x16x32_bf16 v[62:65], v[134:137], v[182:185], v[62:65]
	v_mfma_f32_16x16x32_bf16 v[54:57], v[142:145], v[182:185], v[54:57]
	v_mfma_f32_16x16x32_bf16 v[46:49], v[134:137], v[174:177], v[46:49]
	v_mfma_f32_16x16x32_bf16 v[42:45], v[142:145], v[174:177], v[42:45]
	v_mfma_f32_16x16x32_bf16 v[38:41], v[134:137], v[166:169], v[38:41]
	v_mfma_f32_16x16x32_bf16 v[34:37], v[142:145], v[166:169], v[34:37]
	s_setprio 0
	s_barrier
	ds_read_b128 v[162:165], v224 offset:16384
	ds_read_b128 v[166:169], v224 offset:17408
	ds_read_b128 v[170:173], v224 offset:18432
	ds_read_b128 v[174:177], v224 offset:19456
	ds_read_b128 v[178:181], v224 offset:20480
	ds_read_b128 v[182:185], v224 offset:21504
	ds_read_b128 v[186:189], v224 offset:22528
	ds_read_b128 v[190:193], v224 offset:23552
	s_mov_b32 m0, s37
	s_nop 0
	global_load_lds_dwordx4 v200, s[28:29]
	s_add_u32 s34, s28, 0x80000
	s_mov_b32 m0, s39
	s_nop 0
	global_load_lds_dwordx4 v201, s[28:29]
	s_addc_u32 s35, s29, 0
	s_mov_b32 m0, s38
	s_nop 0
	global_load_lds_dwordx4 v200, s[34:35]
	s_nop 0
	s_mov_b32 m0, s49
	s_nop 0
	global_load_lds_dwordx4 v201, s[34:35]
	s_add_u32 s34, s16, s59
	s_addc_u32 s35, s17, 0
	s_mov_b32 m0, s33
	s_nop 0
	global_load_lds_dwordx4 v215, s[34:35]
	s_nop 0
	s_mov_b32 m0, s41
	s_nop 0
	global_load_lds_dwordx4 v217, s[34:35]
	s_waitcnt vmcnt(8)
	s_waitcnt lgkmcnt(0)
	s_barrier
	s_setprio 1
	v_mfma_f32_16x16x32_bf16 v[94:97], v[146:149], v[162:165], v[94:97]
	v_mfma_f32_16x16x32_bf16 v[90:93], v[154:157], v[162:165], v[90:93]
	v_mfma_f32_16x16x32_bf16 v[86:89], v[146:149], v[170:173], v[86:89]
	v_mfma_f32_16x16x32_bf16 v[82:85], v[154:157], v[170:173], v[82:85]
	v_mfma_f32_16x16x32_bf16 v[74:77], v[146:149], v[178:181], v[74:77]
	v_mfma_f32_16x16x32_bf16 v[66:69], v[154:157], v[178:181], v[66:69]
	v_mfma_f32_16x16x32_bf16 v[58:61], v[146:149], v[186:189], v[58:61]
	v_mfma_f32_16x16x32_bf16 v[50:53], v[154:157], v[186:189], v[50:53]
	v_mfma_f32_16x16x32_bf16 v[94:97], v[150:153], v[166:169], v[94:97]
	v_mfma_f32_16x16x32_bf16 v[90:93], v[158:161], v[166:169], v[90:93]
	v_mfma_f32_16x16x32_bf16 v[86:89], v[150:153], v[174:177], v[86:89]
	v_mfma_f32_16x16x32_bf16 v[82:85], v[158:161], v[174:177], v[82:85]
	v_mfma_f32_16x16x32_bf16 v[74:77], v[150:153], v[182:185], v[74:77]
	v_mfma_f32_16x16x32_bf16 v[66:69], v[158:161], v[182:185], v[66:69]
	v_mfma_f32_16x16x32_bf16 v[58:61], v[150:153], v[190:193], v[58:61]
	v_mfma_f32_16x16x32_bf16 v[50:53], v[158:161], v[190:193], v[50:53]
	v_mfma_f32_16x16x32_bf16 v[30:33], v[130:133], v[162:165], v[30:33]
	v_mfma_f32_16x16x32_bf16 v[26:29], v[138:141], v[162:165], v[26:29]
	v_mfma_f32_16x16x32_bf16 v[22:25], v[130:133], v[170:173], v[22:25]
	v_mfma_f32_16x16x32_bf16 v[18:21], v[138:141], v[170:173], v[18:21]
	v_mfma_f32_16x16x32_bf16 v[14:17], v[130:133], v[178:181], v[14:17]
	v_mfma_f32_16x16x32_bf16 v[10:13], v[138:141], v[178:181], v[10:13]
	v_mfma_f32_16x16x32_bf16 v[6:9], v[130:133], v[186:189], v[6:9]
	v_mfma_f32_16x16x32_bf16 v[2:5], v[138:141], v[186:189], v[2:5]
	v_mfma_f32_16x16x32_bf16 v[30:33], v[134:137], v[166:169], v[30:33]
	v_mfma_f32_16x16x32_bf16 v[26:29], v[142:145], v[166:169], v[26:29]
	v_mfma_f32_16x16x32_bf16 v[22:25], v[134:137], v[174:177], v[22:25]
	v_mfma_f32_16x16x32_bf16 v[18:21], v[142:145], v[174:177], v[18:21]
	v_mfma_f32_16x16x32_bf16 v[14:17], v[134:137], v[182:185], v[14:17]
	v_mfma_f32_16x16x32_bf16 v[10:13], v[142:145], v[182:185], v[10:13]
	v_mfma_f32_16x16x32_bf16 v[6:9], v[134:137], v[190:193], v[6:9]
	v_mfma_f32_16x16x32_bf16 v[2:5], v[142:145], v[190:193], v[2:5]
	s_setprio 0
	s_barrier
	v_add_u32_e32 v142, 0x18000, v221
	v_add_u32_e32 v158, 0x1c000, v221
	ds_read_b128 v[130:133], v142
	ds_read_b128 v[134:137], v142 offset:1024
	ds_read_b128 v[138:141], v142 offset:2048
	ds_read_b128 v[142:145], v142 offset:3072
	ds_read_b128 v[146:149], v158
	ds_read_b128 v[150:153], v158 offset:1024
	ds_read_b128 v[154:157], v158 offset:2048
	ds_read_b128 v[158:161], v158 offset:3072
	ds_read_b128 v[162:165], v224 offset:32768
	ds_read_b128 v[166:169], v224 offset:33792
	ds_read_b128 v[170:173], v224 offset:34816
	ds_read_b128 v[174:177], v224 offset:35840
	ds_read_b128 v[178:181], v224 offset:36864
	ds_read_b128 v[182:185], v224 offset:37888
	ds_read_b128 v[186:189], v224 offset:38912
	ds_read_b128 v[190:193], v224 offset:39936
	s_mov_b32 m0, s40
	s_nop 0
	global_load_lds_dwordx4 v216, s[34:35]
	s_nop 0
	s_mov_b32 m0, s50
	s_nop 0
	global_load_lds_dwordx4 v218, s[34:35]
	s_waitcnt vmcnt(8)
	s_waitcnt lgkmcnt(0)
	s_barrier
	s_setprio 1
	v_mfma_f32_16x16x32_bf16 v[126:129], v[130:133], v[162:165], v[126:129]
	v_mfma_f32_16x16x32_bf16 v[122:125], v[138:141], v[162:165], v[122:125]
	v_mfma_f32_16x16x32_bf16 v[118:121], v[130:133], v[170:173], v[118:121]
	v_mfma_f32_16x16x32_bf16 v[114:117], v[138:141], v[170:173], v[114:117]
	v_mfma_f32_16x16x32_bf16 v[110:113], v[130:133], v[178:181], v[110:113]
	v_mfma_f32_16x16x32_bf16 v[106:109], v[138:141], v[178:181], v[106:109]
	v_mfma_f32_16x16x32_bf16 v[102:105], v[130:133], v[186:189], v[102:105]
	v_mfma_f32_16x16x32_bf16 v[98:101], v[138:141], v[186:189], v[98:101]
	v_mfma_f32_16x16x32_bf16 v[126:129], v[134:137], v[166:169], v[126:129]
	v_mfma_f32_16x16x32_bf16 v[122:125], v[142:145], v[166:169], v[122:125]
	v_mfma_f32_16x16x32_bf16 v[118:121], v[134:137], v[174:177], v[118:121]
	v_mfma_f32_16x16x32_bf16 v[114:117], v[142:145], v[174:177], v[114:117]
	v_mfma_f32_16x16x32_bf16 v[110:113], v[134:137], v[182:185], v[110:113]
	v_mfma_f32_16x16x32_bf16 v[106:109], v[142:145], v[182:185], v[106:109]
	v_mfma_f32_16x16x32_bf16 v[102:105], v[134:137], v[190:193], v[102:105]
	v_mfma_f32_16x16x32_bf16 v[98:101], v[142:145], v[190:193], v[98:101]
	v_mfma_f32_16x16x32_bf16 v[78:81], v[146:149], v[162:165], v[78:81]
	v_mfma_f32_16x16x32_bf16 v[70:73], v[154:157], v[162:165], v[70:73]
	v_mfma_f32_16x16x32_bf16 v[62:65], v[146:149], v[170:173], v[62:65]
	v_mfma_f32_16x16x32_bf16 v[54:57], v[154:157], v[170:173], v[54:57]
	v_mfma_f32_16x16x32_bf16 v[46:49], v[146:149], v[178:181], v[46:49]
	v_mfma_f32_16x16x32_bf16 v[42:45], v[154:157], v[178:181], v[42:45]
	v_mfma_f32_16x16x32_bf16 v[38:41], v[146:149], v[186:189], v[38:41]
	v_mfma_f32_16x16x32_bf16 v[34:37], v[154:157], v[186:189], v[34:37]
	v_mfma_f32_16x16x32_bf16 v[78:81], v[150:153], v[166:169], v[78:81]
	v_mfma_f32_16x16x32_bf16 v[70:73], v[158:161], v[166:169], v[70:73]
	v_mfma_f32_16x16x32_bf16 v[62:65], v[150:153], v[174:177], v[62:65]
	v_mfma_f32_16x16x32_bf16 v[54:57], v[158:161], v[174:177], v[54:57]
	v_mfma_f32_16x16x32_bf16 v[46:49], v[150:153], v[182:185], v[46:49]
	v_mfma_f32_16x16x32_bf16 v[42:45], v[158:161], v[182:185], v[42:45]
	v_mfma_f32_16x16x32_bf16 v[38:41], v[150:153], v[190:193], v[38:41]
	v_mfma_f32_16x16x32_bf16 v[34:37], v[158:161], v[190:193], v[34:37]
	s_setprio 0
	s_barrier
	ds_read_b128 v[162:165], v224 offset:49152
	ds_read_b128 v[166:169], v224 offset:50176
	ds_read_b128 v[170:173], v224 offset:51200
	ds_read_b128 v[174:177], v224 offset:52224
	ds_read_b128 v[178:181], v224 offset:53248
	ds_read_b128 v[182:185], v224 offset:54272
	ds_read_b128 v[186:189], v224 offset:55296
	ds_read_b128 v[190:193], v224 offset:56320
	s_mov_b32 m0, s42
	s_nop 0
	global_load_lds_dwordx4 v200, s[30:31]
	s_add_u32 s28, s28, 0x80080
	s_mov_b32 m0, s51
	s_nop 0
	global_load_lds_dwordx4 v201, s[30:31]
	s_addc_u32 s29, s29, 0
	s_mov_b32 m0, s44
	s_nop 0
	global_load_lds_dwordx4 v200, s[28:29]
	s_nop 0
	s_mov_b32 m0, s52
	s_nop 0
	global_load_lds_dwordx4 v201, s[28:29]
	s_add_u32 s28, s34, 0x80
	s_addc_u32 s29, s35, 0
	s_mov_b32 m0, s43
	s_nop 0
	global_load_lds_dwordx4 v215, s[28:29]
	s_nop 0
	s_mov_b32 m0, s53
	s_nop 0
	global_load_lds_dwordx4 v217, s[28:29]
	s_waitcnt vmcnt(8)
	s_waitcnt lgkmcnt(0)
	s_barrier
	s_setprio 1
	v_mfma_f32_16x16x32_bf16 v[94:97], v[130:133], v[162:165], v[94:97]
	v_mfma_f32_16x16x32_bf16 v[90:93], v[138:141], v[162:165], v[90:93]
	v_mfma_f32_16x16x32_bf16 v[86:89], v[130:133], v[170:173], v[86:89]
	v_mfma_f32_16x16x32_bf16 v[82:85], v[138:141], v[170:173], v[82:85]
	v_mfma_f32_16x16x32_bf16 v[74:77], v[130:133], v[178:181], v[74:77]
	v_mfma_f32_16x16x32_bf16 v[66:69], v[138:141], v[178:181], v[66:69]
	v_mfma_f32_16x16x32_bf16 v[58:61], v[130:133], v[186:189], v[58:61]
	v_mfma_f32_16x16x32_bf16 v[50:53], v[138:141], v[186:189], v[50:53]
	v_mfma_f32_16x16x32_bf16 v[94:97], v[134:137], v[166:169], v[94:97]
	v_mfma_f32_16x16x32_bf16 v[90:93], v[142:145], v[166:169], v[90:93]
	v_mfma_f32_16x16x32_bf16 v[86:89], v[134:137], v[174:177], v[86:89]
	v_mfma_f32_16x16x32_bf16 v[82:85], v[142:145], v[174:177], v[82:85]
	v_mfma_f32_16x16x32_bf16 v[74:77], v[134:137], v[182:185], v[74:77]
	v_mfma_f32_16x16x32_bf16 v[66:69], v[142:145], v[182:185], v[66:69]
	v_mfma_f32_16x16x32_bf16 v[58:61], v[134:137], v[190:193], v[58:61]
	v_mfma_f32_16x16x32_bf16 v[50:53], v[142:145], v[190:193], v[50:53]
	v_mfma_f32_16x16x32_bf16 v[30:33], v[146:149], v[162:165], v[30:33]
	v_mfma_f32_16x16x32_bf16 v[26:29], v[154:157], v[162:165], v[26:29]
	v_mfma_f32_16x16x32_bf16 v[22:25], v[146:149], v[170:173], v[22:25]
	v_mfma_f32_16x16x32_bf16 v[18:21], v[154:157], v[170:173], v[18:21]
	v_mfma_f32_16x16x32_bf16 v[14:17], v[146:149], v[178:181], v[14:17]
	v_mfma_f32_16x16x32_bf16 v[10:13], v[154:157], v[178:181], v[10:13]
	v_mfma_f32_16x16x32_bf16 v[6:9], v[146:149], v[186:189], v[6:9]
	v_mfma_f32_16x16x32_bf16 v[2:5], v[154:157], v[186:189], v[2:5]
	v_mfma_f32_16x16x32_bf16 v[30:33], v[150:153], v[166:169], v[30:33]
	v_mfma_f32_16x16x32_bf16 v[26:29], v[158:161], v[166:169], v[26:29]
	v_mfma_f32_16x16x32_bf16 v[22:25], v[150:153], v[174:177], v[22:25]
	v_mfma_f32_16x16x32_bf16 v[18:21], v[158:161], v[174:177], v[18:21]
	v_mfma_f32_16x16x32_bf16 v[14:17], v[150:153], v[182:185], v[14:17]
	v_mfma_f32_16x16x32_bf16 v[10:13], v[158:161], v[182:185], v[10:13]
	v_mfma_f32_16x16x32_bf16 v[6:9], v[150:153], v[190:193], v[6:9]
	v_mfma_f32_16x16x32_bf16 v[2:5], v[158:161], v[190:193], v[2:5]
	s_setprio 0
	s_barrier
	s_add_i32 s58, s58, 2
	s_add_u32 s26, s26, 0x100
	s_addc_u32 s27, s27, 0
	s_cmp_gt_u32 s58, 29
	s_cbranch_scc1 .LBB0_360

.LBB0_390:
	s_add_u32 s24, s22, 0x100
	s_addc_u32 s25, s23, 0
	s_and_b64 s[28:29], s[26:27], exec
	s_cselect_b32 s59, s24, 0
	s_add_u32 s28, s56, s22
	s_addc_u32 s29, s57, s23
	s_waitcnt vmcnt(8)
	s_and_b64 s[22:23], s[26:27], exec
	s_waitcnt lgkmcnt(0)
	s_cselect_b32 s22, s28, s55
	s_cselect_b32 s23, s29, s54
	s_add_u32 s26, s22, 0x80
	s_addc_u32 s27, s23, 0
	s_barrier
	s_setprio 1
	v_mfma_f32_16x16x32_bf16 v[62:65], v[66:69], v[106:109], v[62:65]
	v_mfma_f32_16x16x32_bf16 v[58:61], v[74:77], v[106:109], v[58:61]
	v_mfma_f32_16x16x32_bf16 v[54:57], v[66:69], v[98:101], v[54:57]
	v_mfma_f32_16x16x32_bf16 v[50:53], v[74:77], v[98:101], v[50:53]
	v_mfma_f32_16x16x32_bf16 v[46:49], v[66:69], v[90:93], v[46:49]
	v_mfma_f32_16x16x32_bf16 v[42:45], v[74:77], v[90:93], v[42:45]
	v_mfma_f32_16x16x32_bf16 v[38:41], v[66:69], v[82:85], v[38:41]
	v_mfma_f32_16x16x32_bf16 v[34:37], v[74:77], v[82:85], v[34:37]
	v_mfma_f32_16x16x32_bf16 v[62:65], v[70:73], v[110:113], v[62:65]
	v_mfma_f32_16x16x32_bf16 v[58:61], v[78:81], v[110:113], v[58:61]
	v_mfma_f32_16x16x32_bf16 v[54:57], v[70:73], v[102:105], v[54:57]
	v_mfma_f32_16x16x32_bf16 v[50:53], v[78:81], v[102:105], v[50:53]
	v_mfma_f32_16x16x32_bf16 v[46:49], v[70:73], v[94:97], v[46:49]
	v_mfma_f32_16x16x32_bf16 v[42:45], v[78:81], v[94:97], v[42:45]
	v_mfma_f32_16x16x32_bf16 v[38:41], v[70:73], v[86:89], v[38:41]
	v_mfma_f32_16x16x32_bf16 v[34:37], v[78:81], v[86:89], v[34:37]
	s_setprio 0
	s_setprio 1
	s_setprio 0
	s_barrier
	ds_read_b128 v[82:85], v126 offset:16384
	ds_read_b128 v[86:89], v126 offset:17408
	ds_read_b128 v[90:93], v126 offset:18432
	ds_read_b128 v[94:97], v126 offset:19456
	ds_read_b128 v[98:101], v126 offset:20480
	ds_read_b128 v[102:105], v126 offset:21504
	ds_read_b128 v[106:109], v126 offset:22528
	ds_read_b128 v[110:113], v126 offset:23552
	s_mov_b32 m0, s35
	s_nop 0
	global_load_lds_dwordx4 v200, s[22:23]
	s_add_u32 s28, s22, 0x80000
	s_mov_b32 m0, s37
	s_nop 0
	global_load_lds_dwordx4 v201, s[22:23]
	s_addc_u32 s29, s23, 0
	s_mov_b32 m0, s36
	s_nop 0
	global_load_lds_dwordx4 v200, s[28:29]
	s_nop 0
	s_mov_b32 m0, s45
	s_nop 0
	global_load_lds_dwordx4 v201, s[28:29]
	s_add_u32 s28, s8, s59
	s_addc_u32 s29, s9, 0
	s_mov_b32 m0, s3
	s_nop 0
	global_load_lds_dwordx4 v121, s[28:29]
	s_nop 0
	s_mov_b32 m0, s39
	s_nop 0
	global_load_lds_dwordx4 v123, s[28:29]
	s_waitcnt vmcnt(8)
	s_waitcnt lgkmcnt(0)
	s_barrier
	s_setprio 1
	v_mfma_f32_16x16x32_bf16 v[30:33], v[66:69], v[82:85], v[30:33]
	v_mfma_f32_16x16x32_bf16 v[26:29], v[74:77], v[82:85], v[26:29]
	v_mfma_f32_16x16x32_bf16 v[22:25], v[66:69], v[90:93], v[22:25]
	v_mfma_f32_16x16x32_bf16 v[18:21], v[74:77], v[90:93], v[18:21]
	v_mfma_f32_16x16x32_bf16 v[14:17], v[66:69], v[98:101], v[14:17]
	v_mfma_f32_16x16x32_bf16 v[10:13], v[74:77], v[98:101], v[10:13]
	v_mfma_f32_16x16x32_bf16 v[6:9], v[66:69], v[106:109], v[6:9]
	v_mfma_f32_16x16x32_bf16 v[2:5], v[74:77], v[106:109], v[2:5]
	v_mfma_f32_16x16x32_bf16 v[30:33], v[70:73], v[86:89], v[30:33]
	v_mfma_f32_16x16x32_bf16 v[26:29], v[78:81], v[86:89], v[26:29]
	v_mfma_f32_16x16x32_bf16 v[22:25], v[70:73], v[94:97], v[22:25]
	v_mfma_f32_16x16x32_bf16 v[18:21], v[78:81], v[94:97], v[18:21]
	v_mfma_f32_16x16x32_bf16 v[14:17], v[70:73], v[102:105], v[14:17]
	v_mfma_f32_16x16x32_bf16 v[10:13], v[78:81], v[102:105], v[10:13]
	v_mfma_f32_16x16x32_bf16 v[6:9], v[70:73], v[110:113], v[6:9]
	v_mfma_f32_16x16x32_bf16 v[2:5], v[78:81], v[110:113], v[2:5]
	s_setprio 0
	s_setprio 1
	s_setprio 0
	s_barrier
	v_add_u32_e32 v78, 0x18000, v114
	ds_read_b128 v[66:69], v78
	ds_read_b128 v[70:73], v78 offset:1024
	ds_read_b128 v[74:77], v78 offset:2048
	ds_read_b128 v[78:81], v78 offset:3072
	ds_read_b128 v[82:85], v126 offset:32768
	ds_read_b128 v[86:89], v126 offset:33792
	ds_read_b128 v[90:93], v126 offset:34816
	ds_read_b128 v[94:97], v126 offset:35840
	ds_read_b128 v[98:101], v126 offset:36864
	ds_read_b128 v[102:105], v126 offset:37888
	ds_read_b128 v[106:109], v126 offset:38912
	ds_read_b128 v[110:113], v126 offset:39936
	s_mov_b32 m0, s38
	s_nop 0
	global_load_lds_dwordx4 v120, s[28:29]
	s_nop 0
	s_mov_b32 m0, s46
	s_nop 0
	global_load_lds_dwordx4 v122, s[28:29]
	s_waitcnt vmcnt(8)
	s_waitcnt lgkmcnt(0)
	s_barrier
	s_setprio 1
	v_mfma_f32_16x16x32_bf16 v[62:65], v[66:69], v[82:85], v[62:65]
	v_mfma_f32_16x16x32_bf16 v[58:61], v[74:77], v[82:85], v[58:61]
	v_mfma_f32_16x16x32_bf16 v[54:57], v[66:69], v[90:93], v[54:57]
	v_mfma_f32_16x16x32_bf16 v[50:53], v[74:77], v[90:93], v[50:53]
	v_mfma_f32_16x16x32_bf16 v[46:49], v[66:69], v[98:101], v[46:49]
	v_mfma_f32_16x16x32_bf16 v[42:45], v[74:77], v[98:101], v[42:45]
	v_mfma_f32_16x16x32_bf16 v[38:41], v[66:69], v[106:109], v[38:41]
	v_mfma_f32_16x16x32_bf16 v[34:37], v[74:77], v[106:109], v[34:37]
	v_mfma_f32_16x16x32_bf16 v[62:65], v[70:73], v[86:89], v[62:65]
	v_mfma_f32_16x16x32_bf16 v[58:61], v[78:81], v[86:89], v[58:61]
	v_mfma_f32_16x16x32_bf16 v[54:57], v[70:73], v[94:97], v[54:57]
	v_mfma_f32_16x16x32_bf16 v[50:53], v[78:81], v[94:97], v[50:53]
	v_mfma_f32_16x16x32_bf16 v[46:49], v[70:73], v[102:105], v[46:49]
	v_mfma_f32_16x16x32_bf16 v[42:45], v[78:81], v[102:105], v[42:45]
	v_mfma_f32_16x16x32_bf16 v[38:41], v[70:73], v[110:113], v[38:41]
	v_mfma_f32_16x16x32_bf16 v[34:37], v[78:81], v[110:113], v[34:37]
	s_setprio 0
	s_setprio 1
	s_setprio 0
	s_barrier
	ds_read_b128 v[82:85], v126 offset:49152
	ds_read_b128 v[86:89], v126 offset:50176
	ds_read_b128 v[90:93], v126 offset:51200
	ds_read_b128 v[94:97], v126 offset:52224
	ds_read_b128 v[98:101], v126 offset:53248
	ds_read_b128 v[102:105], v126 offset:54272
	ds_read_b128 v[106:109], v126 offset:55296
	ds_read_b128 v[110:113], v126 offset:56320
	s_mov_b32 m0, s40
	s_nop 0
	global_load_lds_dwordx4 v200, s[26:27]
	s_add_u32 s22, s22, 0x80080
	s_mov_b32 m0, s47
	s_nop 0
	global_load_lds_dwordx4 v201, s[26:27]
	s_addc_u32 s23, s23, 0
	s_mov_b32 m0, s42
	s_nop 0
	global_load_lds_dwordx4 v200, s[22:23]
	s_nop 0
	s_mov_b32 m0, s48
	s_nop 0
	global_load_lds_dwordx4 v201, s[22:23]
	s_add_u32 s22, s28, 0x80
	s_addc_u32 s23, s29, 0
	s_mov_b32 m0, s41
	s_nop 0
	global_load_lds_dwordx4 v121, s[22:23]
	s_nop 0
	s_mov_b32 m0, s49
	s_nop 0
	global_load_lds_dwordx4 v123, s[22:23]
	s_waitcnt vmcnt(8)
	s_waitcnt lgkmcnt(0)
	s_barrier
	s_setprio 1
	v_mfma_f32_16x16x32_bf16 v[30:33], v[66:69], v[82:85], v[30:33]
	v_mfma_f32_16x16x32_bf16 v[26:29], v[74:77], v[82:85], v[26:29]
	v_mfma_f32_16x16x32_bf16 v[22:25], v[66:69], v[90:93], v[22:25]
	v_mfma_f32_16x16x32_bf16 v[18:21], v[74:77], v[90:93], v[18:21]
	v_mfma_f32_16x16x32_bf16 v[14:17], v[66:69], v[98:101], v[14:17]
	v_mfma_f32_16x16x32_bf16 v[10:13], v[74:77], v[98:101], v[10:13]
	v_mfma_f32_16x16x32_bf16 v[6:9], v[66:69], v[106:109], v[6:9]
	v_mfma_f32_16x16x32_bf16 v[2:5], v[74:77], v[106:109], v[2:5]
	v_mfma_f32_16x16x32_bf16 v[30:33], v[70:73], v[86:89], v[30:33]
	v_mfma_f32_16x16x32_bf16 v[26:29], v[78:81], v[86:89], v[26:29]
	v_mfma_f32_16x16x32_bf16 v[22:25], v[70:73], v[94:97], v[22:25]
	v_mfma_f32_16x16x32_bf16 v[18:21], v[78:81], v[94:97], v[18:21]
	v_mfma_f32_16x16x32_bf16 v[14:17], v[70:73], v[102:105], v[14:17]
	v_mfma_f32_16x16x32_bf16 v[10:13], v[78:81], v[102:105], v[10:13]
	v_mfma_f32_16x16x32_bf16 v[6:9], v[70:73], v[110:113], v[6:9]
	v_mfma_f32_16x16x32_bf16 v[2:5], v[78:81], v[110:113], v[2:5]
	s_setprio 0
	s_setprio 1
	s_setprio 0
	s_barrier
	s_add_i32 s58, s58, 2
	s_cmp_gt_u32 s58, 5
	s_cbranch_scc1 .LBB0_392
	s_mov_b64 s[22:23], s[24:25]
	s_branch .LBB0_388

.LBB0_485:
	s_and_b64 s[38:39], s[10:11], exec
	s_cselect_b32 s71, 0, s8
	s_add_u32 s38, s0, s8
	s_addc_u32 s39, s1, s9
	s_waitcnt vmcnt(8)
	s_and_b64 s[10:11], s[10:11], exec
	s_waitcnt lgkmcnt(0)
	s_cselect_b32 s10, s40, s38
	s_cselect_b32 s11, s35, s39
	s_add_u32 s38, s10, 0x80
	s_addc_u32 s39, s11, 0
	s_barrier
	s_setprio 1
	v_mfma_f32_16x16x32_bf16 v[126:129], v[146:149], v[186:189], v[126:129]
	v_mfma_f32_16x16x32_bf16 v[122:125], v[154:157], v[186:189], v[122:125]
	v_mfma_f32_16x16x32_bf16 v[110:113], v[146:149], v[178:181], v[110:113]
	v_mfma_f32_16x16x32_bf16 v[106:109], v[154:157], v[178:181], v[106:109]
	v_mfma_f32_16x16x32_bf16 v[94:97], v[146:149], v[170:173], v[94:97]
	v_mfma_f32_16x16x32_bf16 v[90:93], v[154:157], v[170:173], v[90:93]
	v_mfma_f32_16x16x32_bf16 v[78:81], v[146:149], v[162:165], v[78:81]
	v_mfma_f32_16x16x32_bf16 v[74:77], v[154:157], v[162:165], v[74:77]
	v_mfma_f32_16x16x32_bf16 v[126:129], v[150:153], v[190:193], v[126:129]
	v_mfma_f32_16x16x32_bf16 v[122:125], v[158:161], v[190:193], v[122:125]
	v_mfma_f32_16x16x32_bf16 v[110:113], v[150:153], v[182:185], v[110:113]
	v_mfma_f32_16x16x32_bf16 v[106:109], v[158:161], v[182:185], v[106:109]
	v_mfma_f32_16x16x32_bf16 v[94:97], v[150:153], v[174:177], v[94:97]
	v_mfma_f32_16x16x32_bf16 v[90:93], v[158:161], v[174:177], v[90:93]
	v_mfma_f32_16x16x32_bf16 v[78:81], v[150:153], v[166:169], v[78:81]
	v_mfma_f32_16x16x32_bf16 v[74:77], v[158:161], v[166:169], v[74:77]
	v_mfma_f32_16x16x32_bf16 v[118:121], v[130:133], v[186:189], v[118:121]
	v_mfma_f32_16x16x32_bf16 v[114:117], v[138:141], v[186:189], v[114:117]
	v_mfma_f32_16x16x32_bf16 v[102:105], v[130:133], v[178:181], v[102:105]
	v_mfma_f32_16x16x32_bf16 v[98:101], v[138:141], v[178:181], v[98:101]
	v_mfma_f32_16x16x32_bf16 v[86:89], v[130:133], v[170:173], v[86:89]
	v_mfma_f32_16x16x32_bf16 v[82:85], v[138:141], v[170:173], v[82:85]
	v_mfma_f32_16x16x32_bf16 v[70:73], v[130:133], v[162:165], v[70:73]
	v_mfma_f32_16x16x32_bf16 v[66:69], v[138:141], v[162:165], v[66:69]
	v_mfma_f32_16x16x32_bf16 v[118:121], v[134:137], v[190:193], v[118:121]
	v_mfma_f32_16x16x32_bf16 v[114:117], v[142:145], v[190:193], v[114:117]
	v_mfma_f32_16x16x32_bf16 v[102:105], v[134:137], v[182:185], v[102:105]
	v_mfma_f32_16x16x32_bf16 v[98:101], v[142:145], v[182:185], v[98:101]
	v_mfma_f32_16x16x32_bf16 v[86:89], v[134:137], v[174:177], v[86:89]
	v_mfma_f32_16x16x32_bf16 v[82:85], v[142:145], v[174:177], v[82:85]
	v_mfma_f32_16x16x32_bf16 v[70:73], v[134:137], v[166:169], v[70:73]
	v_mfma_f32_16x16x32_bf16 v[66:69], v[142:145], v[166:169], v[66:69]
	s_setprio 0
	s_barrier
	ds_read_b128 v[162:165], v231 offset:16384
	ds_read_b128 v[166:169], v231 offset:17408
	ds_read_b128 v[170:173], v231 offset:18432
	ds_read_b128 v[174:177], v231 offset:19456
	ds_read_b128 v[178:181], v231 offset:20480
	ds_read_b128 v[182:185], v231 offset:21504
	ds_read_b128 v[186:189], v231 offset:22528
	ds_read_b128 v[190:193], v231 offset:23552
	s_mov_b32 m0, s48
	s_nop 0
	global_load_lds_dwordx4 v203, s[10:11]
	s_add_u32 s42, s10, 0x20000
	s_mov_b32 m0, s49
	s_nop 0
	global_load_lds_dwordx4 v204, s[10:11]
	s_addc_u32 s43, s11, 0
	s_mov_b32 m0, s50
	s_nop 0
	global_load_lds_dwordx4 v203, s[42:43]
	s_nop 0
	s_mov_b32 m0, s51
	s_nop 0
	global_load_lds_dwordx4 v204, s[42:43]
	s_add_u32 s42, s24, s71
	s_addc_u32 s43, s25, 0
	s_mov_b32 m0, s47
	s_nop 0
	global_load_lds_dwordx4 v221, s[42:43]
	s_nop 0
	s_mov_b32 m0, s52
	s_nop 0
	global_load_lds_dwordx4 v223, s[42:43]
	s_waitcnt vmcnt(8)
	s_waitcnt lgkmcnt(0)
	s_barrier
	s_setprio 1
	v_mfma_f32_16x16x32_bf16 v[62:65], v[146:149], v[162:165], v[62:65]
	v_mfma_f32_16x16x32_bf16 v[58:61], v[154:157], v[162:165], v[58:61]
	v_mfma_f32_16x16x32_bf16 v[46:49], v[146:149], v[170:173], v[46:49]
	v_mfma_f32_16x16x32_bf16 v[42:45], v[154:157], v[170:173], v[42:45]
	v_mfma_f32_16x16x32_bf16 v[30:33], v[146:149], v[178:181], v[30:33]
	v_mfma_f32_16x16x32_bf16 v[26:29], v[154:157], v[178:181], v[26:29]
	v_mfma_f32_16x16x32_bf16 v[14:17], v[146:149], v[186:189], v[14:17]
	v_mfma_f32_16x16x32_bf16 v[10:13], v[154:157], v[186:189], v[10:13]
	v_mfma_f32_16x16x32_bf16 v[62:65], v[150:153], v[166:169], v[62:65]
	v_mfma_f32_16x16x32_bf16 v[58:61], v[158:161], v[166:169], v[58:61]
	v_mfma_f32_16x16x32_bf16 v[46:49], v[150:153], v[174:177], v[46:49]
	v_mfma_f32_16x16x32_bf16 v[42:45], v[158:161], v[174:177], v[42:45]
	v_mfma_f32_16x16x32_bf16 v[30:33], v[150:153], v[182:185], v[30:33]
	v_mfma_f32_16x16x32_bf16 v[26:29], v[158:161], v[182:185], v[26:29]
	v_mfma_f32_16x16x32_bf16 v[14:17], v[150:153], v[190:193], v[14:17]
	v_mfma_f32_16x16x32_bf16 v[10:13], v[158:161], v[190:193], v[10:13]
	v_mfma_f32_16x16x32_bf16 v[54:57], v[130:133], v[162:165], v[54:57]
	v_mfma_f32_16x16x32_bf16 v[50:53], v[138:141], v[162:165], v[50:53]
	v_mfma_f32_16x16x32_bf16 v[38:41], v[130:133], v[170:173], v[38:41]
	v_mfma_f32_16x16x32_bf16 v[34:37], v[138:141], v[170:173], v[34:37]
	v_mfma_f32_16x16x32_bf16 v[22:25], v[130:133], v[178:181], v[22:25]
	v_mfma_f32_16x16x32_bf16 v[18:21], v[138:141], v[178:181], v[18:21]
	v_mfma_f32_16x16x32_bf16 v[6:9], v[130:133], v[186:189], v[6:9]
	v_mfma_f32_16x16x32_bf16 v[2:5], v[138:141], v[186:189], v[2:5]
	v_mfma_f32_16x16x32_bf16 v[54:57], v[134:137], v[166:169], v[54:57]
	v_mfma_f32_16x16x32_bf16 v[50:53], v[142:145], v[166:169], v[50:53]
	v_mfma_f32_16x16x32_bf16 v[38:41], v[134:137], v[174:177], v[38:41]
	v_mfma_f32_16x16x32_bf16 v[34:37], v[142:145], v[174:177], v[34:37]
	v_mfma_f32_16x16x32_bf16 v[22:25], v[134:137], v[182:185], v[22:25]
	v_mfma_f32_16x16x32_bf16 v[18:21], v[142:145], v[182:185], v[18:21]
	v_mfma_f32_16x16x32_bf16 v[6:9], v[134:137], v[190:193], v[6:9]
	v_mfma_f32_16x16x32_bf16 v[2:5], v[142:145], v[190:193], v[2:5]
	s_setprio 0
	s_barrier
	v_add_u32_e32 v142, 0x18000, v228
	v_add_u32_e32 v158, 0x1c000, v228
	ds_read_b128 v[130:133], v142
	ds_read_b128 v[134:137], v142 offset:1024
	ds_read_b128 v[138:141], v142 offset:2048
	ds_read_b128 v[142:145], v142 offset:3072
	ds_read_b128 v[146:149], v158
	ds_read_b128 v[150:153], v158 offset:1024
	ds_read_b128 v[154:157], v158 offset:2048
	ds_read_b128 v[158:161], v158 offset:3072
	ds_read_b128 v[162:165], v231 offset:32768
	ds_read_b128 v[166:169], v231 offset:33792
	ds_read_b128 v[170:173], v231 offset:34816
	ds_read_b128 v[174:177], v231 offset:35840
	ds_read_b128 v[178:181], v231 offset:36864
	ds_read_b128 v[182:185], v231 offset:37888
	ds_read_b128 v[186:189], v231 offset:38912
	ds_read_b128 v[190:193], v231 offset:39936
	s_mov_b32 m0, s53
	s_nop 0
	global_load_lds_dwordx4 v222, s[42:43]
	s_nop 0
	s_mov_b32 m0, s54
	s_nop 0
	global_load_lds_dwordx4 v224, s[42:43]
	s_waitcnt vmcnt(8)
	s_waitcnt lgkmcnt(0)
	s_barrier
	s_setprio 1
	v_mfma_f32_16x16x32_bf16 v[126:129], v[130:133], v[162:165], v[126:129]
	v_mfma_f32_16x16x32_bf16 v[122:125], v[138:141], v[162:165], v[122:125]
	v_mfma_f32_16x16x32_bf16 v[110:113], v[130:133], v[170:173], v[110:113]
	v_mfma_f32_16x16x32_bf16 v[106:109], v[138:141], v[170:173], v[106:109]
	v_mfma_f32_16x16x32_bf16 v[94:97], v[130:133], v[178:181], v[94:97]
	v_mfma_f32_16x16x32_bf16 v[90:93], v[138:141], v[178:181], v[90:93]
	v_mfma_f32_16x16x32_bf16 v[78:81], v[130:133], v[186:189], v[78:81]
	v_mfma_f32_16x16x32_bf16 v[74:77], v[138:141], v[186:189], v[74:77]
	v_mfma_f32_16x16x32_bf16 v[126:129], v[134:137], v[166:169], v[126:129]
	v_mfma_f32_16x16x32_bf16 v[122:125], v[142:145], v[166:169], v[122:125]
	v_mfma_f32_16x16x32_bf16 v[110:113], v[134:137], v[174:177], v[110:113]
	v_mfma_f32_16x16x32_bf16 v[106:109], v[142:145], v[174:177], v[106:109]
	v_mfma_f32_16x16x32_bf16 v[94:97], v[134:137], v[182:185], v[94:97]
	v_mfma_f32_16x16x32_bf16 v[90:93], v[142:145], v[182:185], v[90:93]
	v_mfma_f32_16x16x32_bf16 v[78:81], v[134:137], v[190:193], v[78:81]
	v_mfma_f32_16x16x32_bf16 v[74:77], v[142:145], v[190:193], v[74:77]
	v_mfma_f32_16x16x32_bf16 v[118:121], v[146:149], v[162:165], v[118:121]
	v_mfma_f32_16x16x32_bf16 v[114:117], v[154:157], v[162:165], v[114:117]
	v_mfma_f32_16x16x32_bf16 v[102:105], v[146:149], v[170:173], v[102:105]
	v_mfma_f32_16x16x32_bf16 v[98:101], v[154:157], v[170:173], v[98:101]
	v_mfma_f32_16x16x32_bf16 v[86:89], v[146:149], v[178:181], v[86:89]
	v_mfma_f32_16x16x32_bf16 v[82:85], v[154:157], v[178:181], v[82:85]
	v_mfma_f32_16x16x32_bf16 v[70:73], v[146:149], v[186:189], v[70:73]
	v_mfma_f32_16x16x32_bf16 v[66:69], v[154:157], v[186:189], v[66:69]
	v_mfma_f32_16x16x32_bf16 v[118:121], v[150:153], v[166:169], v[118:121]
	v_mfma_f32_16x16x32_bf16 v[114:117], v[158:161], v[166:169], v[114:117]
	v_mfma_f32_16x16x32_bf16 v[102:105], v[150:153], v[174:177], v[102:105]
	v_mfma_f32_16x16x32_bf16 v[98:101], v[158:161], v[174:177], v[98:101]
	v_mfma_f32_16x16x32_bf16 v[86:89], v[150:153], v[182:185], v[86:89]
	v_mfma_f32_16x16x32_bf16 v[82:85], v[158:161], v[182:185], v[82:85]
	v_mfma_f32_16x16x32_bf16 v[70:73], v[150:153], v[190:193], v[70:73]
	v_mfma_f32_16x16x32_bf16 v[66:69], v[158:161], v[190:193], v[66:69]
	s_setprio 0
	s_barrier
	ds_read_b128 v[162:165], v231 offset:49152
	ds_read_b128 v[166:169], v231 offset:50176
	ds_read_b128 v[170:173], v231 offset:51200
	ds_read_b128 v[174:177], v231 offset:52224
	ds_read_b128 v[178:181], v231 offset:53248
	ds_read_b128 v[182:185], v231 offset:54272
	ds_read_b128 v[186:189], v231 offset:55296
	ds_read_b128 v[190:193], v231 offset:56320
	s_mov_b32 m0, s55
	s_nop 0
	global_load_lds_dwordx4 v203, s[38:39]
	s_add_u32 s10, s10, 0x20080
	s_mov_b32 m0, s56
	s_nop 0
	global_load_lds_dwordx4 v204, s[38:39]
	s_addc_u32 s11, s11, 0
	s_mov_b32 m0, s59
	s_nop 0
	global_load_lds_dwordx4 v203, s[10:11]
	s_nop 0
	s_mov_b32 m0, s60
	s_nop 0
	global_load_lds_dwordx4 v204, s[10:11]
	s_add_u32 s10, s42, 0x80
	s_addc_u32 s11, s43, 0
	s_mov_b32 m0, s57
	s_nop 0
	global_load_lds_dwordx4 v221, s[10:11]
	s_nop 0
	s_mov_b32 m0, s58
	s_nop 0
	global_load_lds_dwordx4 v223, s[10:11]
	s_waitcnt vmcnt(8)
	s_waitcnt lgkmcnt(0)
	s_barrier
	s_setprio 1
	v_mfma_f32_16x16x32_bf16 v[62:65], v[130:133], v[162:165], v[62:65]
	v_mfma_f32_16x16x32_bf16 v[58:61], v[138:141], v[162:165], v[58:61]
	v_mfma_f32_16x16x32_bf16 v[46:49], v[130:133], v[170:173], v[46:49]
	v_mfma_f32_16x16x32_bf16 v[42:45], v[138:141], v[170:173], v[42:45]
	v_mfma_f32_16x16x32_bf16 v[30:33], v[130:133], v[178:181], v[30:33]
	v_mfma_f32_16x16x32_bf16 v[26:29], v[138:141], v[178:181], v[26:29]
	v_mfma_f32_16x16x32_bf16 v[14:17], v[130:133], v[186:189], v[14:17]
	v_mfma_f32_16x16x32_bf16 v[10:13], v[138:141], v[186:189], v[10:13]
	v_mfma_f32_16x16x32_bf16 v[62:65], v[134:137], v[166:169], v[62:65]
	v_mfma_f32_16x16x32_bf16 v[58:61], v[142:145], v[166:169], v[58:61]
	v_mfma_f32_16x16x32_bf16 v[46:49], v[134:137], v[174:177], v[46:49]
	v_mfma_f32_16x16x32_bf16 v[42:45], v[142:145], v[174:177], v[42:45]
	v_mfma_f32_16x16x32_bf16 v[30:33], v[134:137], v[182:185], v[30:33]
	v_mfma_f32_16x16x32_bf16 v[26:29], v[142:145], v[182:185], v[26:29]
	v_mfma_f32_16x16x32_bf16 v[14:17], v[134:137], v[190:193], v[14:17]
	v_mfma_f32_16x16x32_bf16 v[10:13], v[142:145], v[190:193], v[10:13]
	v_mfma_f32_16x16x32_bf16 v[54:57], v[146:149], v[162:165], v[54:57]
	v_mfma_f32_16x16x32_bf16 v[50:53], v[154:157], v[162:165], v[50:53]
	v_mfma_f32_16x16x32_bf16 v[38:41], v[146:149], v[170:173], v[38:41]
	v_mfma_f32_16x16x32_bf16 v[34:37], v[154:157], v[170:173], v[34:37]
	v_mfma_f32_16x16x32_bf16 v[22:25], v[146:149], v[178:181], v[22:25]
	v_mfma_f32_16x16x32_bf16 v[18:21], v[154:157], v[178:181], v[18:21]
	v_mfma_f32_16x16x32_bf16 v[6:9], v[146:149], v[186:189], v[6:9]
	v_mfma_f32_16x16x32_bf16 v[2:5], v[154:157], v[186:189], v[2:5]
	v_mfma_f32_16x16x32_bf16 v[54:57], v[150:153], v[166:169], v[54:57]
	v_mfma_f32_16x16x32_bf16 v[50:53], v[158:161], v[166:169], v[50:53]
	v_mfma_f32_16x16x32_bf16 v[38:41], v[150:153], v[174:177], v[38:41]
	v_mfma_f32_16x16x32_bf16 v[34:37], v[158:161], v[174:177], v[34:37]
	v_mfma_f32_16x16x32_bf16 v[22:25], v[150:153], v[182:185], v[22:25]
	v_mfma_f32_16x16x32_bf16 v[18:21], v[158:161], v[182:185], v[18:21]
	v_mfma_f32_16x16x32_bf16 v[6:9], v[150:153], v[190:193], v[6:9]
	v_mfma_f32_16x16x32_bf16 v[2:5], v[158:161], v[190:193], v[2:5]
	s_setprio 0
	s_barrier
	s_add_i32 s41, s41, 2
	s_add_u32 s8, s8, 0x100
	s_addc_u32 s9, s9, 0
	s_cmp_gt_u32 s41, 5
	s_cbranch_scc1 .LBB0_490

.LBB0_547:
	s_and_b64 s[36:37], s[34:35], exec
	s_cselect_b32 s65, 0, s8
	s_add_u32 s36, s0, s8
	s_addc_u32 s37, s1, s9
	s_waitcnt vmcnt(8)
	s_and_b64 s[34:35], s[34:35], exec
	s_waitcnt lgkmcnt(0)
	s_cselect_b32 s34, s40, s36
	s_cselect_b32 s35, s29, s37
	s_add_u32 s36, s34, 0x80
	s_addc_u32 s37, s35, 0
	s_barrier
	s_setprio 1
	v_mfma_f32_16x16x32_bf16 v[126:129], v[146:149], v[186:189], v[126:129]
	v_mfma_f32_16x16x32_bf16 v[122:125], v[154:157], v[186:189], v[122:125]
	v_mfma_f32_16x16x32_bf16 v[118:121], v[146:149], v[178:181], v[118:121]
	v_mfma_f32_16x16x32_bf16 v[110:113], v[154:157], v[178:181], v[110:113]
	v_mfma_f32_16x16x32_bf16 v[102:105], v[146:149], v[170:173], v[102:105]
	v_mfma_f32_16x16x32_bf16 v[94:97], v[154:157], v[170:173], v[94:97]
	v_mfma_f32_16x16x32_bf16 v[86:89], v[146:149], v[162:165], v[86:89]
	v_mfma_f32_16x16x32_bf16 v[78:81], v[154:157], v[162:165], v[78:81]
	v_mfma_f32_16x16x32_bf16 v[126:129], v[150:153], v[190:193], v[126:129]
	v_mfma_f32_16x16x32_bf16 v[122:125], v[158:161], v[190:193], v[122:125]
	v_mfma_f32_16x16x32_bf16 v[118:121], v[150:153], v[182:185], v[118:121]
	v_mfma_f32_16x16x32_bf16 v[110:113], v[158:161], v[182:185], v[110:113]
	v_mfma_f32_16x16x32_bf16 v[102:105], v[150:153], v[174:177], v[102:105]
	v_mfma_f32_16x16x32_bf16 v[94:97], v[158:161], v[174:177], v[94:97]
	v_mfma_f32_16x16x32_bf16 v[86:89], v[150:153], v[166:169], v[86:89]
	v_mfma_f32_16x16x32_bf16 v[78:81], v[158:161], v[166:169], v[78:81]
	v_mfma_f32_16x16x32_bf16 v[114:117], v[130:133], v[186:189], v[114:117]
	v_mfma_f32_16x16x32_bf16 v[106:109], v[138:141], v[186:189], v[106:109]
	v_mfma_f32_16x16x32_bf16 v[98:101], v[130:133], v[178:181], v[98:101]
	v_mfma_f32_16x16x32_bf16 v[90:93], v[138:141], v[178:181], v[90:93]
	v_mfma_f32_16x16x32_bf16 v[82:85], v[130:133], v[170:173], v[82:85]
	v_mfma_f32_16x16x32_bf16 v[74:77], v[138:141], v[170:173], v[74:77]
	v_mfma_f32_16x16x32_bf16 v[70:73], v[130:133], v[162:165], v[70:73]
	v_mfma_f32_16x16x32_bf16 v[66:69], v[138:141], v[162:165], v[66:69]
	v_mfma_f32_16x16x32_bf16 v[114:117], v[134:137], v[190:193], v[114:117]
	v_mfma_f32_16x16x32_bf16 v[106:109], v[142:145], v[190:193], v[106:109]
	v_mfma_f32_16x16x32_bf16 v[98:101], v[134:137], v[182:185], v[98:101]
	v_mfma_f32_16x16x32_bf16 v[90:93], v[142:145], v[182:185], v[90:93]
	v_mfma_f32_16x16x32_bf16 v[82:85], v[134:137], v[174:177], v[82:85]
	v_mfma_f32_16x16x32_bf16 v[74:77], v[142:145], v[174:177], v[74:77]
	v_mfma_f32_16x16x32_bf16 v[70:73], v[134:137], v[166:169], v[70:73]
	v_mfma_f32_16x16x32_bf16 v[66:69], v[142:145], v[166:169], v[66:69]
	s_setprio 0
	s_barrier
	ds_read_b128 v[162:165], v225 offset:16384
	ds_read_b128 v[166:169], v225 offset:17408
	ds_read_b128 v[170:173], v225 offset:18432
	ds_read_b128 v[174:177], v225 offset:19456
	ds_read_b128 v[178:181], v225 offset:20480
	ds_read_b128 v[182:185], v225 offset:21504
	ds_read_b128 v[186:189], v225 offset:22528
	ds_read_b128 v[190:193], v225 offset:23552
	s_mov_b32 m0, s46
	s_nop 0
	global_load_lds_dwordx4 v203, s[34:35]
	s_add_u32 s38, s34, 0x20000
	s_mov_b32 m0, s48
	s_nop 0
	global_load_lds_dwordx4 v204, s[34:35]
	s_addc_u32 s39, s35, 0
	s_mov_b32 m0, s47
	s_nop 0
	global_load_lds_dwordx4 v203, s[38:39]
	s_nop 0
	s_mov_b32 m0, s57
	s_nop 0
	global_load_lds_dwordx4 v204, s[38:39]
	s_add_u32 s38, s26, s65
	s_addc_u32 s39, s27, 0
	s_mov_b32 m0, s45
	s_nop 0
	global_load_lds_dwordx4 v215, s[38:39]
	s_nop 0
	s_mov_b32 m0, s50
	s_nop 0
	global_load_lds_dwordx4 v217, s[38:39]
	s_waitcnt vmcnt(8)
	s_waitcnt lgkmcnt(0)
	s_barrier
	s_setprio 1
	v_mfma_f32_16x16x32_bf16 v[62:65], v[146:149], v[162:165], v[62:65]
	v_mfma_f32_16x16x32_bf16 v[58:61], v[154:157], v[162:165], v[58:61]
	v_mfma_f32_16x16x32_bf16 v[54:57], v[146:149], v[170:173], v[54:57]
	v_mfma_f32_16x16x32_bf16 v[46:49], v[154:157], v[170:173], v[46:49]
	v_mfma_f32_16x16x32_bf16 v[38:41], v[146:149], v[178:181], v[38:41]
	v_mfma_f32_16x16x32_bf16 v[30:33], v[154:157], v[178:181], v[30:33]
	v_mfma_f32_16x16x32_bf16 v[22:25], v[146:149], v[186:189], v[22:25]
	v_mfma_f32_16x16x32_bf16 v[14:17], v[154:157], v[186:189], v[14:17]
	v_mfma_f32_16x16x32_bf16 v[62:65], v[150:153], v[166:169], v[62:65]
	v_mfma_f32_16x16x32_bf16 v[58:61], v[158:161], v[166:169], v[58:61]
	v_mfma_f32_16x16x32_bf16 v[54:57], v[150:153], v[174:177], v[54:57]
	v_mfma_f32_16x16x32_bf16 v[46:49], v[158:161], v[174:177], v[46:49]
	v_mfma_f32_16x16x32_bf16 v[38:41], v[150:153], v[182:185], v[38:41]
	v_mfma_f32_16x16x32_bf16 v[30:33], v[158:161], v[182:185], v[30:33]
	v_mfma_f32_16x16x32_bf16 v[22:25], v[150:153], v[190:193], v[22:25]
	v_mfma_f32_16x16x32_bf16 v[14:17], v[158:161], v[190:193], v[14:17]
	v_mfma_f32_16x16x32_bf16 v[50:53], v[130:133], v[162:165], v[50:53]
	v_mfma_f32_16x16x32_bf16 v[42:45], v[138:141], v[162:165], v[42:45]
	v_mfma_f32_16x16x32_bf16 v[34:37], v[130:133], v[170:173], v[34:37]
	v_mfma_f32_16x16x32_bf16 v[26:29], v[138:141], v[170:173], v[26:29]
	v_mfma_f32_16x16x32_bf16 v[18:21], v[130:133], v[178:181], v[18:21]
	v_mfma_f32_16x16x32_bf16 v[10:13], v[138:141], v[178:181], v[10:13]
	v_mfma_f32_16x16x32_bf16 v[6:9], v[130:133], v[186:189], v[6:9]
	v_mfma_f32_16x16x32_bf16 v[2:5], v[138:141], v[186:189], v[2:5]
	v_mfma_f32_16x16x32_bf16 v[50:53], v[134:137], v[166:169], v[50:53]
	v_mfma_f32_16x16x32_bf16 v[42:45], v[142:145], v[166:169], v[42:45]
	v_mfma_f32_16x16x32_bf16 v[34:37], v[134:137], v[174:177], v[34:37]
	v_mfma_f32_16x16x32_bf16 v[26:29], v[142:145], v[174:177], v[26:29]
	v_mfma_f32_16x16x32_bf16 v[18:21], v[134:137], v[182:185], v[18:21]
	v_mfma_f32_16x16x32_bf16 v[10:13], v[142:145], v[182:185], v[10:13]
	v_mfma_f32_16x16x32_bf16 v[6:9], v[134:137], v[190:193], v[6:9]
	v_mfma_f32_16x16x32_bf16 v[2:5], v[142:145], v[190:193], v[2:5]
	s_setprio 0
	s_barrier
	v_add_u32_e32 v142, 0x18000, v222
	v_add_u32_e32 v158, 0x1c000, v222
	ds_read_b128 v[130:133], v142
	ds_read_b128 v[134:137], v142 offset:1024
	ds_read_b128 v[138:141], v142 offset:2048
	ds_read_b128 v[142:145], v142 offset:3072
	ds_read_b128 v[146:149], v158
	ds_read_b128 v[150:153], v158 offset:1024
	ds_read_b128 v[154:157], v158 offset:2048
	ds_read_b128 v[158:161], v158 offset:3072
	ds_read_b128 v[162:165], v225 offset:32768
	ds_read_b128 v[166:169], v225 offset:33792
	ds_read_b128 v[170:173], v225 offset:34816
	ds_read_b128 v[174:177], v225 offset:35840
	ds_read_b128 v[178:181], v225 offset:36864
	ds_read_b128 v[182:185], v225 offset:37888
	ds_read_b128 v[186:189], v225 offset:38912
	ds_read_b128 v[190:193], v225 offset:39936
	s_mov_b32 m0, s49
	s_nop 0
	global_load_lds_dwordx4 v216, s[38:39]
	s_nop 0
	s_mov_b32 m0, s58
	s_nop 0
	global_load_lds_dwordx4 v218, s[38:39]
	s_waitcnt vmcnt(8)
	s_waitcnt lgkmcnt(0)
	s_barrier
	s_setprio 1
	v_mfma_f32_16x16x32_bf16 v[126:129], v[130:133], v[162:165], v[126:129]
	v_mfma_f32_16x16x32_bf16 v[122:125], v[138:141], v[162:165], v[122:125]
	v_mfma_f32_16x16x32_bf16 v[118:121], v[130:133], v[170:173], v[118:121]
	v_mfma_f32_16x16x32_bf16 v[110:113], v[138:141], v[170:173], v[110:113]
	v_mfma_f32_16x16x32_bf16 v[102:105], v[130:133], v[178:181], v[102:105]
	v_mfma_f32_16x16x32_bf16 v[94:97], v[138:141], v[178:181], v[94:97]
	v_mfma_f32_16x16x32_bf16 v[86:89], v[130:133], v[186:189], v[86:89]
	v_mfma_f32_16x16x32_bf16 v[78:81], v[138:141], v[186:189], v[78:81]
	v_mfma_f32_16x16x32_bf16 v[126:129], v[134:137], v[166:169], v[126:129]
	v_mfma_f32_16x16x32_bf16 v[122:125], v[142:145], v[166:169], v[122:125]
	v_mfma_f32_16x16x32_bf16 v[118:121], v[134:137], v[174:177], v[118:121]
	v_mfma_f32_16x16x32_bf16 v[110:113], v[142:145], v[174:177], v[110:113]
	v_mfma_f32_16x16x32_bf16 v[102:105], v[134:137], v[182:185], v[102:105]
	v_mfma_f32_16x16x32_bf16 v[94:97], v[142:145], v[182:185], v[94:97]
	v_mfma_f32_16x16x32_bf16 v[86:89], v[134:137], v[190:193], v[86:89]
	v_mfma_f32_16x16x32_bf16 v[78:81], v[142:145], v[190:193], v[78:81]
	v_mfma_f32_16x16x32_bf16 v[114:117], v[146:149], v[162:165], v[114:117]
	v_mfma_f32_16x16x32_bf16 v[106:109], v[154:157], v[162:165], v[106:109]
	v_mfma_f32_16x16x32_bf16 v[98:101], v[146:149], v[170:173], v[98:101]
	v_mfma_f32_16x16x32_bf16 v[90:93], v[154:157], v[170:173], v[90:93]
	v_mfma_f32_16x16x32_bf16 v[82:85], v[146:149], v[178:181], v[82:85]
	v_mfma_f32_16x16x32_bf16 v[74:77], v[154:157], v[178:181], v[74:77]
	v_mfma_f32_16x16x32_bf16 v[70:73], v[146:149], v[186:189], v[70:73]
	v_mfma_f32_16x16x32_bf16 v[66:69], v[154:157], v[186:189], v[66:69]
	v_mfma_f32_16x16x32_bf16 v[114:117], v[150:153], v[166:169], v[114:117]
	v_mfma_f32_16x16x32_bf16 v[106:109], v[158:161], v[166:169], v[106:109]
	v_mfma_f32_16x16x32_bf16 v[98:101], v[150:153], v[174:177], v[98:101]
	v_mfma_f32_16x16x32_bf16 v[90:93], v[158:161], v[174:177], v[90:93]
	v_mfma_f32_16x16x32_bf16 v[82:85], v[150:153], v[182:185], v[82:85]
	v_mfma_f32_16x16x32_bf16 v[74:77], v[158:161], v[182:185], v[74:77]
	v_mfma_f32_16x16x32_bf16 v[70:73], v[150:153], v[190:193], v[70:73]
	v_mfma_f32_16x16x32_bf16 v[66:69], v[158:161], v[190:193], v[66:69]
	s_setprio 0
	s_barrier
	ds_read_b128 v[162:165], v225 offset:49152
	ds_read_b128 v[166:169], v225 offset:50176
	ds_read_b128 v[170:173], v225 offset:51200
	ds_read_b128 v[174:177], v225 offset:52224
	ds_read_b128 v[178:181], v225 offset:53248
	ds_read_b128 v[182:185], v225 offset:54272
	ds_read_b128 v[186:189], v225 offset:55296
	ds_read_b128 v[190:193], v225 offset:56320
	s_mov_b32 m0, s51
	s_nop 0
	global_load_lds_dwordx4 v203, s[36:37]
	s_add_u32 s34, s34, 0x20080
	s_mov_b32 m0, s59
	s_nop 0
	global_load_lds_dwordx4 v204, s[36:37]
	s_addc_u32 s35, s35, 0
	s_mov_b32 m0, s53
	s_nop 0
	global_load_lds_dwordx4 v203, s[34:35]
	s_nop 0
	s_mov_b32 m0, s60
	s_nop 0
	global_load_lds_dwordx4 v204, s[34:35]
	s_add_u32 s34, s38, 0x80
	s_addc_u32 s35, s39, 0
	s_mov_b32 m0, s52
	s_nop 0
	global_load_lds_dwordx4 v215, s[34:35]
	s_nop 0
	s_mov_b32 m0, s61
	s_nop 0
	global_load_lds_dwordx4 v217, s[34:35]
	s_waitcnt vmcnt(8)
	s_waitcnt lgkmcnt(0)
	s_barrier
	s_setprio 1
	v_mfma_f32_16x16x32_bf16 v[62:65], v[130:133], v[162:165], v[62:65]
	v_mfma_f32_16x16x32_bf16 v[58:61], v[138:141], v[162:165], v[58:61]
	v_mfma_f32_16x16x32_bf16 v[54:57], v[130:133], v[170:173], v[54:57]
	v_mfma_f32_16x16x32_bf16 v[46:49], v[138:141], v[170:173], v[46:49]
	v_mfma_f32_16x16x32_bf16 v[38:41], v[130:133], v[178:181], v[38:41]
	v_mfma_f32_16x16x32_bf16 v[30:33], v[138:141], v[178:181], v[30:33]
	v_mfma_f32_16x16x32_bf16 v[22:25], v[130:133], v[186:189], v[22:25]
	v_mfma_f32_16x16x32_bf16 v[14:17], v[138:141], v[186:189], v[14:17]
	v_mfma_f32_16x16x32_bf16 v[62:65], v[134:137], v[166:169], v[62:65]
	v_mfma_f32_16x16x32_bf16 v[58:61], v[142:145], v[166:169], v[58:61]
	v_mfma_f32_16x16x32_bf16 v[54:57], v[134:137], v[174:177], v[54:57]
	v_mfma_f32_16x16x32_bf16 v[46:49], v[142:145], v[174:177], v[46:49]
	v_mfma_f32_16x16x32_bf16 v[38:41], v[134:137], v[182:185], v[38:41]
	v_mfma_f32_16x16x32_bf16 v[30:33], v[142:145], v[182:185], v[30:33]
	v_mfma_f32_16x16x32_bf16 v[22:25], v[134:137], v[190:193], v[22:25]
	v_mfma_f32_16x16x32_bf16 v[14:17], v[142:145], v[190:193], v[14:17]
	v_mfma_f32_16x16x32_bf16 v[50:53], v[146:149], v[162:165], v[50:53]
	v_mfma_f32_16x16x32_bf16 v[42:45], v[154:157], v[162:165], v[42:45]
	v_mfma_f32_16x16x32_bf16 v[34:37], v[146:149], v[170:173], v[34:37]
	v_mfma_f32_16x16x32_bf16 v[26:29], v[154:157], v[170:173], v[26:29]
	v_mfma_f32_16x16x32_bf16 v[18:21], v[146:149], v[178:181], v[18:21]
	v_mfma_f32_16x16x32_bf16 v[10:13], v[154:157], v[178:181], v[10:13]
	v_mfma_f32_16x16x32_bf16 v[6:9], v[146:149], v[186:189], v[6:9]
	v_mfma_f32_16x16x32_bf16 v[2:5], v[154:157], v[186:189], v[2:5]
	v_mfma_f32_16x16x32_bf16 v[50:53], v[150:153], v[166:169], v[50:53]
	v_mfma_f32_16x16x32_bf16 v[42:45], v[158:161], v[166:169], v[42:45]
	v_mfma_f32_16x16x32_bf16 v[34:37], v[150:153], v[174:177], v[34:37]
	v_mfma_f32_16x16x32_bf16 v[26:29], v[158:161], v[174:177], v[26:29]
	v_mfma_f32_16x16x32_bf16 v[18:21], v[150:153], v[182:185], v[18:21]
	v_mfma_f32_16x16x32_bf16 v[10:13], v[158:161], v[182:185], v[10:13]
	v_mfma_f32_16x16x32_bf16 v[6:9], v[150:153], v[190:193], v[6:9]
	v_mfma_f32_16x16x32_bf16 v[2:5], v[158:161], v[190:193], v[2:5]
	s_setprio 0
	s_barrier
	s_add_i32 s41, s41, 2
	s_add_u32 s8, s8, 0x100
	s_addc_u32 s9, s9, 0
	s_cmp_gt_u32 s41, 5
	s_cbranch_scc1 .LBB0_538

.LBB0_578:
	s_add_u32 s6, s0, 0x100
	s_addc_u32 s7, s1, 0
	s_and_b64 s[26:27], s[24:25], exec
	s_cselect_b32 s56, s6, 0
	s_add_u32 s26, s41, s0
	s_addc_u32 s27, s54, s1
	s_waitcnt vmcnt(8)
	s_and_b64 s[0:1], s[24:25], exec
	s_waitcnt lgkmcnt(0)
	s_cselect_b32 s0, s26, s40
	s_cselect_b32 s1, s27, s21
	s_add_u32 s24, s0, 0x80
	s_addc_u32 s25, s1, 0
	s_barrier
	s_setprio 1
	v_mfma_f32_16x16x32_bf16 v[126:129], v[146:149], v[186:189], v[126:129]
	v_mfma_f32_16x16x32_bf16 v[122:125], v[154:157], v[186:189], v[122:125]
	v_mfma_f32_16x16x32_bf16 v[118:121], v[146:149], v[178:181], v[118:121]
	v_mfma_f32_16x16x32_bf16 v[114:117], v[154:157], v[178:181], v[114:117]
	v_mfma_f32_16x16x32_bf16 v[110:113], v[146:149], v[170:173], v[110:113]
	v_mfma_f32_16x16x32_bf16 v[106:109], v[154:157], v[170:173], v[106:109]
	v_mfma_f32_16x16x32_bf16 v[102:105], v[146:149], v[162:165], v[102:105]
	v_mfma_f32_16x16x32_bf16 v[98:101], v[154:157], v[162:165], v[98:101]
	v_mfma_f32_16x16x32_bf16 v[126:129], v[150:153], v[190:193], v[126:129]
	v_mfma_f32_16x16x32_bf16 v[122:125], v[158:161], v[190:193], v[122:125]
	v_mfma_f32_16x16x32_bf16 v[118:121], v[150:153], v[182:185], v[118:121]
	v_mfma_f32_16x16x32_bf16 v[114:117], v[158:161], v[182:185], v[114:117]
	v_mfma_f32_16x16x32_bf16 v[110:113], v[150:153], v[174:177], v[110:113]
	v_mfma_f32_16x16x32_bf16 v[106:109], v[158:161], v[174:177], v[106:109]
	v_mfma_f32_16x16x32_bf16 v[102:105], v[150:153], v[166:169], v[102:105]
	v_mfma_f32_16x16x32_bf16 v[98:101], v[158:161], v[166:169], v[98:101]
	v_mfma_f32_16x16x32_bf16 v[62:65], v[130:133], v[186:189], v[62:65]
	v_mfma_f32_16x16x32_bf16 v[58:61], v[138:141], v[186:189], v[58:61]
	v_mfma_f32_16x16x32_bf16 v[54:57], v[130:133], v[178:181], v[54:57]
	v_mfma_f32_16x16x32_bf16 v[50:53], v[138:141], v[178:181], v[50:53]
	v_mfma_f32_16x16x32_bf16 v[46:49], v[130:133], v[170:173], v[46:49]
	v_mfma_f32_16x16x32_bf16 v[42:45], v[138:141], v[170:173], v[42:45]
	v_mfma_f32_16x16x32_bf16 v[38:41], v[130:133], v[162:165], v[38:41]
	v_mfma_f32_16x16x32_bf16 v[34:37], v[138:141], v[162:165], v[34:37]
	v_mfma_f32_16x16x32_bf16 v[62:65], v[134:137], v[190:193], v[62:65]
	v_mfma_f32_16x16x32_bf16 v[58:61], v[142:145], v[190:193], v[58:61]
	v_mfma_f32_16x16x32_bf16 v[54:57], v[134:137], v[182:185], v[54:57]
	v_mfma_f32_16x16x32_bf16 v[50:53], v[142:145], v[182:185], v[50:53]
	v_mfma_f32_16x16x32_bf16 v[46:49], v[134:137], v[174:177], v[46:49]
	v_mfma_f32_16x16x32_bf16 v[42:45], v[142:145], v[174:177], v[42:45]
	v_mfma_f32_16x16x32_bf16 v[38:41], v[134:137], v[166:169], v[38:41]
	v_mfma_f32_16x16x32_bf16 v[34:37], v[142:145], v[166:169], v[34:37]
	s_setprio 0
	s_barrier
	ds_read_b128 v[162:165], v216 offset:16384
	ds_read_b128 v[166:169], v216 offset:17408
	ds_read_b128 v[170:173], v216 offset:18432
	ds_read_b128 v[174:177], v216 offset:19456
	ds_read_b128 v[178:181], v216 offset:20480
	ds_read_b128 v[182:185], v216 offset:21504
	ds_read_b128 v[186:189], v216 offset:22528
	ds_read_b128 v[190:193], v216 offset:23552
	s_mov_b32 m0, s30
	s_nop 0
	global_load_lds_dwordx4 v203, s[0:1]
	s_add_u32 s26, s0, 0x20000
	s_mov_b32 m0, s34
	s_nop 0
	global_load_lds_dwordx4 v204, s[0:1]
	s_addc_u32 s27, s1, 0
	s_mov_b32 m0, s31
	s_nop 0
	global_load_lds_dwordx4 v203, s[26:27]
	s_nop 0
	s_mov_b32 m0, s46
	s_nop 0
	global_load_lds_dwordx4 v204, s[26:27]
	s_add_u32 s26, s10, s56
	s_addc_u32 s27, s11, 0
	s_mov_b32 m0, s29
	s_nop 0
	global_load_lds_dwordx4 v212, s[26:27]
	s_nop 0
	s_mov_b32 m0, s36
	s_nop 0
	global_load_lds_dwordx4 v213, s[26:27]
	s_waitcnt vmcnt(8)
	s_waitcnt lgkmcnt(0)
	s_barrier
	s_setprio 1
	v_mfma_f32_16x16x32_bf16 v[94:97], v[146:149], v[162:165], v[94:97]
	v_mfma_f32_16x16x32_bf16 v[90:93], v[154:157], v[162:165], v[90:93]
	v_mfma_f32_16x16x32_bf16 v[86:89], v[146:149], v[170:173], v[86:89]
	v_mfma_f32_16x16x32_bf16 v[82:85], v[154:157], v[170:173], v[82:85]
	v_mfma_f32_16x16x32_bf16 v[78:81], v[146:149], v[178:181], v[78:81]
	v_mfma_f32_16x16x32_bf16 v[74:77], v[154:157], v[178:181], v[74:77]
	v_mfma_f32_16x16x32_bf16 v[70:73], v[146:149], v[186:189], v[70:73]
	v_mfma_f32_16x16x32_bf16 v[66:69], v[154:157], v[186:189], v[66:69]
	v_mfma_f32_16x16x32_bf16 v[94:97], v[150:153], v[166:169], v[94:97]
	v_mfma_f32_16x16x32_bf16 v[90:93], v[158:161], v[166:169], v[90:93]
	v_mfma_f32_16x16x32_bf16 v[86:89], v[150:153], v[174:177], v[86:89]
	v_mfma_f32_16x16x32_bf16 v[82:85], v[158:161], v[174:177], v[82:85]
	v_mfma_f32_16x16x32_bf16 v[78:81], v[150:153], v[182:185], v[78:81]
	v_mfma_f32_16x16x32_bf16 v[74:77], v[158:161], v[182:185], v[74:77]
	v_mfma_f32_16x16x32_bf16 v[70:73], v[150:153], v[190:193], v[70:73]
	v_mfma_f32_16x16x32_bf16 v[66:69], v[158:161], v[190:193], v[66:69]
	v_mfma_f32_16x16x32_bf16 v[30:33], v[130:133], v[162:165], v[30:33]
	v_mfma_f32_16x16x32_bf16 v[26:29], v[138:141], v[162:165], v[26:29]
	v_mfma_f32_16x16x32_bf16 v[22:25], v[130:133], v[170:173], v[22:25]
	v_mfma_f32_16x16x32_bf16 v[18:21], v[138:141], v[170:173], v[18:21]
	v_mfma_f32_16x16x32_bf16 v[14:17], v[130:133], v[178:181], v[14:17]
	v_mfma_f32_16x16x32_bf16 v[10:13], v[138:141], v[178:181], v[10:13]
	v_mfma_f32_16x16x32_bf16 v[6:9], v[130:133], v[186:189], v[6:9]
	v_mfma_f32_16x16x32_bf16 v[2:5], v[138:141], v[186:189], v[2:5]
	v_mfma_f32_16x16x32_bf16 v[30:33], v[134:137], v[166:169], v[30:33]
	v_mfma_f32_16x16x32_bf16 v[26:29], v[142:145], v[166:169], v[26:29]
	v_mfma_f32_16x16x32_bf16 v[22:25], v[134:137], v[174:177], v[22:25]
	v_mfma_f32_16x16x32_bf16 v[18:21], v[142:145], v[174:177], v[18:21]
	v_mfma_f32_16x16x32_bf16 v[14:17], v[134:137], v[182:185], v[14:17]
	v_mfma_f32_16x16x32_bf16 v[10:13], v[142:145], v[182:185], v[10:13]
	v_mfma_f32_16x16x32_bf16 v[6:9], v[134:137], v[190:193], v[6:9]
	v_mfma_f32_16x16x32_bf16 v[2:5], v[142:145], v[190:193], v[2:5]
	s_setprio 0
	s_barrier
	v_add_u32_e32 v142, 0x18000, v210
	v_add_u32_e32 v158, 0x1c000, v210
	ds_read_b128 v[130:133], v142
	ds_read_b128 v[134:137], v142 offset:1024
	ds_read_b128 v[138:141], v142 offset:2048
	ds_read_b128 v[142:145], v142 offset:3072
	ds_read_b128 v[146:149], v158
	ds_read_b128 v[150:153], v158 offset:1024
	ds_read_b128 v[154:157], v158 offset:2048
	ds_read_b128 v[158:161], v158 offset:3072
	ds_read_b128 v[162:165], v216 offset:32768
	ds_read_b128 v[166:169], v216 offset:33792
	ds_read_b128 v[170:173], v216 offset:34816
	ds_read_b128 v[174:177], v216 offset:35840
	ds_read_b128 v[178:181], v216 offset:36864
	ds_read_b128 v[182:185], v216 offset:37888
	ds_read_b128 v[186:189], v216 offset:38912
	ds_read_b128 v[190:193], v216 offset:39936
	s_mov_b32 m0, s35
	s_nop 0
	global_load_lds_dwordx4 v211, s[26:27]
	s_nop 0
	s_mov_b32 m0, s47
	s_nop 0
	global_load_lds_dwordx4 v208, s[26:27]
	s_waitcnt vmcnt(8)
	s_waitcnt lgkmcnt(0)
	s_barrier
	s_setprio 1
	v_mfma_f32_16x16x32_bf16 v[126:129], v[130:133], v[162:165], v[126:129]
	v_mfma_f32_16x16x32_bf16 v[122:125], v[138:141], v[162:165], v[122:125]
	v_mfma_f32_16x16x32_bf16 v[118:121], v[130:133], v[170:173], v[118:121]
	v_mfma_f32_16x16x32_bf16 v[114:117], v[138:141], v[170:173], v[114:117]
	v_mfma_f32_16x16x32_bf16 v[110:113], v[130:133], v[178:181], v[110:113]
	v_mfma_f32_16x16x32_bf16 v[106:109], v[138:141], v[178:181], v[106:109]
	v_mfma_f32_16x16x32_bf16 v[102:105], v[130:133], v[186:189], v[102:105]
	v_mfma_f32_16x16x32_bf16 v[98:101], v[138:141], v[186:189], v[98:101]
	v_mfma_f32_16x16x32_bf16 v[126:129], v[134:137], v[166:169], v[126:129]
	v_mfma_f32_16x16x32_bf16 v[122:125], v[142:145], v[166:169], v[122:125]
	v_mfma_f32_16x16x32_bf16 v[118:121], v[134:137], v[174:177], v[118:121]
	v_mfma_f32_16x16x32_bf16 v[114:117], v[142:145], v[174:177], v[114:117]
	v_mfma_f32_16x16x32_bf16 v[110:113], v[134:137], v[182:185], v[110:113]
	v_mfma_f32_16x16x32_bf16 v[106:109], v[142:145], v[182:185], v[106:109]
	v_mfma_f32_16x16x32_bf16 v[102:105], v[134:137], v[190:193], v[102:105]
	v_mfma_f32_16x16x32_bf16 v[98:101], v[142:145], v[190:193], v[98:101]
	v_mfma_f32_16x16x32_bf16 v[62:65], v[146:149], v[162:165], v[62:65]
	v_mfma_f32_16x16x32_bf16 v[58:61], v[154:157], v[162:165], v[58:61]
	v_mfma_f32_16x16x32_bf16 v[54:57], v[146:149], v[170:173], v[54:57]
	v_mfma_f32_16x16x32_bf16 v[50:53], v[154:157], v[170:173], v[50:53]
	v_mfma_f32_16x16x32_bf16 v[46:49], v[146:149], v[178:181], v[46:49]
	v_mfma_f32_16x16x32_bf16 v[42:45], v[154:157], v[178:181], v[42:45]
	v_mfma_f32_16x16x32_bf16 v[38:41], v[146:149], v[186:189], v[38:41]
	v_mfma_f32_16x16x32_bf16 v[34:37], v[154:157], v[186:189], v[34:37]
	v_mfma_f32_16x16x32_bf16 v[62:65], v[150:153], v[166:169], v[62:65]
	v_mfma_f32_16x16x32_bf16 v[58:61], v[158:161], v[166:169], v[58:61]
	v_mfma_f32_16x16x32_bf16 v[54:57], v[150:153], v[174:177], v[54:57]
	v_mfma_f32_16x16x32_bf16 v[50:53], v[158:161], v[174:177], v[50:53]
	v_mfma_f32_16x16x32_bf16 v[46:49], v[150:153], v[182:185], v[46:49]
	v_mfma_f32_16x16x32_bf16 v[42:45], v[158:161], v[182:185], v[42:45]
	v_mfma_f32_16x16x32_bf16 v[38:41], v[150:153], v[190:193], v[38:41]
	v_mfma_f32_16x16x32_bf16 v[34:37], v[158:161], v[190:193], v[34:37]
	s_setprio 0
	s_barrier
	ds_read_b128 v[162:165], v216 offset:49152
	ds_read_b128 v[166:169], v216 offset:50176
	ds_read_b128 v[170:173], v216 offset:51200
	ds_read_b128 v[174:177], v216 offset:52224
	ds_read_b128 v[178:181], v216 offset:53248
	ds_read_b128 v[182:185], v216 offset:54272
	ds_read_b128 v[186:189], v216 offset:55296
	ds_read_b128 v[190:193], v216 offset:56320
	s_mov_b32 m0, s37
	s_nop 0
	global_load_lds_dwordx4 v203, s[24:25]
	s_add_u32 s0, s0, 0x20080
	s_mov_b32 m0, s48
	s_nop 0
	global_load_lds_dwordx4 v204, s[24:25]
	s_addc_u32 s1, s1, 0
	s_mov_b32 m0, s39
	s_nop 0
	global_load_lds_dwordx4 v203, s[0:1]
	s_nop 0
	s_mov_b32 m0, s49
	s_nop 0
	global_load_lds_dwordx4 v204, s[0:1]
	s_add_u32 s0, s26, 0x80
	s_addc_u32 s1, s27, 0
	s_mov_b32 m0, s38
	s_nop 0
	global_load_lds_dwordx4 v212, s[0:1]
	s_nop 0
	s_mov_b32 m0, s50
	s_nop 0
	global_load_lds_dwordx4 v213, s[0:1]
	s_waitcnt vmcnt(8)
	s_waitcnt lgkmcnt(0)
	s_barrier
	s_setprio 1
	v_mfma_f32_16x16x32_bf16 v[94:97], v[130:133], v[162:165], v[94:97]
	v_mfma_f32_16x16x32_bf16 v[90:93], v[138:141], v[162:165], v[90:93]
	v_mfma_f32_16x16x32_bf16 v[86:89], v[130:133], v[170:173], v[86:89]
	v_mfma_f32_16x16x32_bf16 v[82:85], v[138:141], v[170:173], v[82:85]
	v_mfma_f32_16x16x32_bf16 v[78:81], v[130:133], v[178:181], v[78:81]
	v_mfma_f32_16x16x32_bf16 v[74:77], v[138:141], v[178:181], v[74:77]
	v_mfma_f32_16x16x32_bf16 v[70:73], v[130:133], v[186:189], v[70:73]
	v_mfma_f32_16x16x32_bf16 v[66:69], v[138:141], v[186:189], v[66:69]
	v_mfma_f32_16x16x32_bf16 v[94:97], v[134:137], v[166:169], v[94:97]
	v_mfma_f32_16x16x32_bf16 v[90:93], v[142:145], v[166:169], v[90:93]
	v_mfma_f32_16x16x32_bf16 v[86:89], v[134:137], v[174:177], v[86:89]
	v_mfma_f32_16x16x32_bf16 v[82:85], v[142:145], v[174:177], v[82:85]
	v_mfma_f32_16x16x32_bf16 v[78:81], v[134:137], v[182:185], v[78:81]
	v_mfma_f32_16x16x32_bf16 v[74:77], v[142:145], v[182:185], v[74:77]
	v_mfma_f32_16x16x32_bf16 v[70:73], v[134:137], v[190:193], v[70:73]
	v_mfma_f32_16x16x32_bf16 v[66:69], v[142:145], v[190:193], v[66:69]
	v_mfma_f32_16x16x32_bf16 v[30:33], v[146:149], v[162:165], v[30:33]
	v_mfma_f32_16x16x32_bf16 v[26:29], v[154:157], v[162:165], v[26:29]
	v_mfma_f32_16x16x32_bf16 v[22:25], v[146:149], v[170:173], v[22:25]
	v_mfma_f32_16x16x32_bf16 v[18:21], v[154:157], v[170:173], v[18:21]
	v_mfma_f32_16x16x32_bf16 v[14:17], v[146:149], v[178:181], v[14:17]
	v_mfma_f32_16x16x32_bf16 v[10:13], v[154:157], v[178:181], v[10:13]
	v_mfma_f32_16x16x32_bf16 v[6:9], v[146:149], v[186:189], v[6:9]
	v_mfma_f32_16x16x32_bf16 v[2:5], v[154:157], v[186:189], v[2:5]
	v_mfma_f32_16x16x32_bf16 v[30:33], v[150:153], v[166:169], v[30:33]
	v_mfma_f32_16x16x32_bf16 v[26:29], v[158:161], v[166:169], v[26:29]
	v_mfma_f32_16x16x32_bf16 v[22:25], v[150:153], v[174:177], v[22:25]
	v_mfma_f32_16x16x32_bf16 v[18:21], v[158:161], v[174:177], v[18:21]
	v_mfma_f32_16x16x32_bf16 v[14:17], v[150:153], v[182:185], v[14:17]
	v_mfma_f32_16x16x32_bf16 v[10:13], v[158:161], v[182:185], v[10:13]
	v_mfma_f32_16x16x32_bf16 v[6:9], v[150:153], v[190:193], v[6:9]
	v_mfma_f32_16x16x32_bf16 v[2:5], v[158:161], v[190:193], v[2:5]
	s_setprio 0
	s_barrier
	s_add_i32 s55, s55, 2
	s_cmp_gt_u32 s55, 5
	s_cbranch_scc1 .LBB0_568
	s_mov_b64 s[0:1], s[6:7]
	s_branch .LBB0_576

.LBB0_997:
	s_add_u32 s18, s16, 0x100
	s_addc_u32 s19, s17, 0
	s_and_b64 s[22:23], s[20:21], exec
	s_cselect_b32 s53, s18, 0
	s_add_u32 s22, s50, s16
	s_addc_u32 s23, s51, s17
	s_waitcnt vmcnt(8)
	s_and_b64 s[16:17], s[20:21], exec
	s_waitcnt lgkmcnt(0)
	s_cselect_b32 s16, s22, s49
	s_cselect_b32 s17, s23, s13
	s_add_u32 s20, s16, 0x80
	s_addc_u32 s21, s17, 0
	s_barrier
	s_setprio 1
	v_mfma_f32_16x16x32_bf16 v[126:129], v[146:149], v[186:189], v[126:129]
	v_mfma_f32_16x16x32_bf16 v[122:125], v[154:157], v[186:189], v[122:125]
	v_mfma_f32_16x16x32_bf16 v[118:121], v[146:149], v[178:181], v[118:121]
	v_mfma_f32_16x16x32_bf16 v[114:117], v[154:157], v[178:181], v[114:117]
	v_mfma_f32_16x16x32_bf16 v[94:97], v[146:149], v[170:173], v[94:97]
	v_mfma_f32_16x16x32_bf16 v[90:93], v[154:157], v[170:173], v[90:93]
	v_mfma_f32_16x16x32_bf16 v[86:89], v[146:149], v[162:165], v[86:89]
	v_mfma_f32_16x16x32_bf16 v[78:81], v[154:157], v[162:165], v[78:81]
	v_mfma_f32_16x16x32_bf16 v[126:129], v[150:153], v[190:193], v[126:129]
	v_mfma_f32_16x16x32_bf16 v[122:125], v[158:161], v[190:193], v[122:125]
	v_mfma_f32_16x16x32_bf16 v[118:121], v[150:153], v[182:185], v[118:121]
	v_mfma_f32_16x16x32_bf16 v[114:117], v[158:161], v[182:185], v[114:117]
	v_mfma_f32_16x16x32_bf16 v[94:97], v[150:153], v[174:177], v[94:97]
	v_mfma_f32_16x16x32_bf16 v[90:93], v[158:161], v[174:177], v[90:93]
	v_mfma_f32_16x16x32_bf16 v[86:89], v[150:153], v[166:169], v[86:89]
	v_mfma_f32_16x16x32_bf16 v[78:81], v[158:161], v[166:169], v[78:81]
	v_mfma_f32_16x16x32_bf16 v[110:113], v[130:133], v[186:189], v[110:113]
	v_mfma_f32_16x16x32_bf16 v[106:109], v[138:141], v[186:189], v[106:109]
	v_mfma_f32_16x16x32_bf16 v[102:105], v[130:133], v[178:181], v[102:105]
	v_mfma_f32_16x16x32_bf16 v[98:101], v[138:141], v[178:181], v[98:101]
	v_mfma_f32_16x16x32_bf16 v[82:85], v[130:133], v[170:173], v[82:85]
	v_mfma_f32_16x16x32_bf16 v[74:77], v[138:141], v[170:173], v[74:77]
	v_mfma_f32_16x16x32_bf16 v[70:73], v[130:133], v[162:165], v[70:73]
	v_mfma_f32_16x16x32_bf16 v[66:69], v[138:141], v[162:165], v[66:69]
	v_mfma_f32_16x16x32_bf16 v[110:113], v[134:137], v[190:193], v[110:113]
	v_mfma_f32_16x16x32_bf16 v[106:109], v[142:145], v[190:193], v[106:109]
	v_mfma_f32_16x16x32_bf16 v[102:105], v[134:137], v[182:185], v[102:105]
	v_mfma_f32_16x16x32_bf16 v[98:101], v[142:145], v[182:185], v[98:101]
	v_mfma_f32_16x16x32_bf16 v[82:85], v[134:137], v[174:177], v[82:85]
	v_mfma_f32_16x16x32_bf16 v[74:77], v[142:145], v[174:177], v[74:77]
	v_mfma_f32_16x16x32_bf16 v[70:73], v[134:137], v[166:169], v[70:73]
	v_mfma_f32_16x16x32_bf16 v[66:69], v[142:145], v[166:169], v[66:69]
	s_setprio 0
	s_barrier
	ds_read_b128 v[162:165], v211 offset:16384
	ds_read_b128 v[166:169], v211 offset:17408
	ds_read_b128 v[170:173], v211 offset:18432
	ds_read_b128 v[174:177], v211 offset:19456
	ds_read_b128 v[178:181], v211 offset:20480
	ds_read_b128 v[182:185], v211 offset:21504
	ds_read_b128 v[186:189], v211 offset:22528
	ds_read_b128 v[190:193], v211 offset:23552
	s_mov_b32 m0, s29
	s_nop 0
	global_load_lds_dwordx4 v196, s[16:17]
	s_add_u32 s22, s16, 0x80000
	s_mov_b32 m0, s30
	s_nop 0
	global_load_lds_dwordx4 v197, s[16:17]
	s_addc_u32 s23, s17, 0
	s_mov_b32 m0, s34
	s_nop 0
	global_load_lds_dwordx4 v196, s[22:23]
	s_nop 0
	s_mov_b32 m0, s35
	s_nop 0
	global_load_lds_dwordx4 v197, s[22:23]
	s_add_u32 s22, s6, s53
	s_addc_u32 s23, s7, 0
	s_mov_b32 m0, s28
	s_nop 0
	global_load_lds_dwordx4 v202, s[22:23]
	s_nop 0
	s_mov_b32 m0, s36
	s_nop 0
	global_load_lds_dwordx4 v204, s[22:23]
	s_waitcnt vmcnt(8)
	s_waitcnt lgkmcnt(0)
	s_barrier
	s_setprio 1
	v_mfma_f32_16x16x32_bf16 v[62:65], v[146:149], v[162:165], v[62:65]
	v_mfma_f32_16x16x32_bf16 v[58:61], v[154:157], v[162:165], v[58:61]
	v_mfma_f32_16x16x32_bf16 v[54:57], v[146:149], v[170:173], v[54:57]
	v_mfma_f32_16x16x32_bf16 v[46:49], v[154:157], v[170:173], v[46:49]
	v_mfma_f32_16x16x32_bf16 v[38:41], v[146:149], v[178:181], v[38:41]
	v_mfma_f32_16x16x32_bf16 v[30:33], v[154:157], v[178:181], v[30:33]
	v_mfma_f32_16x16x32_bf16 v[22:25], v[146:149], v[186:189], v[22:25]
	v_mfma_f32_16x16x32_bf16 v[14:17], v[154:157], v[186:189], v[14:17]
	v_mfma_f32_16x16x32_bf16 v[62:65], v[150:153], v[166:169], v[62:65]
	v_mfma_f32_16x16x32_bf16 v[58:61], v[158:161], v[166:169], v[58:61]
	v_mfma_f32_16x16x32_bf16 v[54:57], v[150:153], v[174:177], v[54:57]
	v_mfma_f32_16x16x32_bf16 v[46:49], v[158:161], v[174:177], v[46:49]
	v_mfma_f32_16x16x32_bf16 v[38:41], v[150:153], v[182:185], v[38:41]
	v_mfma_f32_16x16x32_bf16 v[30:33], v[158:161], v[182:185], v[30:33]
	v_mfma_f32_16x16x32_bf16 v[22:25], v[150:153], v[190:193], v[22:25]
	v_mfma_f32_16x16x32_bf16 v[14:17], v[158:161], v[190:193], v[14:17]
	v_mfma_f32_16x16x32_bf16 v[50:53], v[130:133], v[162:165], v[50:53]
	v_mfma_f32_16x16x32_bf16 v[42:45], v[138:141], v[162:165], v[42:45]
	v_mfma_f32_16x16x32_bf16 v[34:37], v[130:133], v[170:173], v[34:37]
	v_mfma_f32_16x16x32_bf16 v[26:29], v[138:141], v[170:173], v[26:29]
	v_mfma_f32_16x16x32_bf16 v[18:21], v[130:133], v[178:181], v[18:21]
	v_mfma_f32_16x16x32_bf16 v[10:13], v[138:141], v[178:181], v[10:13]
	v_mfma_f32_16x16x32_bf16 v[6:9], v[130:133], v[186:189], v[6:9]
	v_mfma_f32_16x16x32_bf16 v[2:5], v[138:141], v[186:189], v[2:5]
	v_mfma_f32_16x16x32_bf16 v[50:53], v[134:137], v[166:169], v[50:53]
	v_mfma_f32_16x16x32_bf16 v[42:45], v[142:145], v[166:169], v[42:45]
	v_mfma_f32_16x16x32_bf16 v[34:37], v[134:137], v[174:177], v[34:37]
	v_mfma_f32_16x16x32_bf16 v[26:29], v[142:145], v[174:177], v[26:29]
	v_mfma_f32_16x16x32_bf16 v[18:21], v[134:137], v[182:185], v[18:21]
	v_mfma_f32_16x16x32_bf16 v[10:13], v[142:145], v[182:185], v[10:13]
	v_mfma_f32_16x16x32_bf16 v[6:9], v[134:137], v[190:193], v[6:9]
	v_mfma_f32_16x16x32_bf16 v[2:5], v[142:145], v[190:193], v[2:5]
	s_setprio 0
	s_barrier
	v_add_u32_e32 v142, 0x18000, v208
	v_add_u32_e32 v158, 0x1c000, v208
	ds_read_b128 v[130:133], v142
	ds_read_b128 v[134:137], v142 offset:1024
	ds_read_b128 v[138:141], v142 offset:2048
	ds_read_b128 v[142:145], v142 offset:3072
	ds_read_b128 v[146:149], v158
	ds_read_b128 v[150:153], v158 offset:1024
	ds_read_b128 v[154:157], v158 offset:2048
	ds_read_b128 v[158:161], v158 offset:3072
	ds_read_b128 v[162:165], v211 offset:32768
	ds_read_b128 v[166:169], v211 offset:33792
	ds_read_b128 v[170:173], v211 offset:34816
	ds_read_b128 v[174:177], v211 offset:35840
	ds_read_b128 v[178:181], v211 offset:36864
	ds_read_b128 v[182:185], v211 offset:37888
	ds_read_b128 v[186:189], v211 offset:38912
	ds_read_b128 v[190:193], v211 offset:39936
	s_mov_b32 m0, s37
	s_nop 0
	global_load_lds_dwordx4 v201, s[22:23]
	s_nop 0
	s_mov_b32 m0, s38
	s_nop 0
	global_load_lds_dwordx4 v203, s[22:23]
	s_waitcnt vmcnt(8)
	s_waitcnt lgkmcnt(0)
	s_barrier
	s_setprio 1
	v_mfma_f32_16x16x32_bf16 v[126:129], v[130:133], v[162:165], v[126:129]
	v_mfma_f32_16x16x32_bf16 v[122:125], v[138:141], v[162:165], v[122:125]
	v_mfma_f32_16x16x32_bf16 v[118:121], v[130:133], v[170:173], v[118:121]
	v_mfma_f32_16x16x32_bf16 v[114:117], v[138:141], v[170:173], v[114:117]
	v_mfma_f32_16x16x32_bf16 v[94:97], v[130:133], v[178:181], v[94:97]
	v_mfma_f32_16x16x32_bf16 v[90:93], v[138:141], v[178:181], v[90:93]
	v_mfma_f32_16x16x32_bf16 v[86:89], v[130:133], v[186:189], v[86:89]
	v_mfma_f32_16x16x32_bf16 v[78:81], v[138:141], v[186:189], v[78:81]
	v_mfma_f32_16x16x32_bf16 v[126:129], v[134:137], v[166:169], v[126:129]
	v_mfma_f32_16x16x32_bf16 v[122:125], v[142:145], v[166:169], v[122:125]
	v_mfma_f32_16x16x32_bf16 v[118:121], v[134:137], v[174:177], v[118:121]
	v_mfma_f32_16x16x32_bf16 v[114:117], v[142:145], v[174:177], v[114:117]
	v_mfma_f32_16x16x32_bf16 v[94:97], v[134:137], v[182:185], v[94:97]
	v_mfma_f32_16x16x32_bf16 v[90:93], v[142:145], v[182:185], v[90:93]
	v_mfma_f32_16x16x32_bf16 v[86:89], v[134:137], v[190:193], v[86:89]
	v_mfma_f32_16x16x32_bf16 v[78:81], v[142:145], v[190:193], v[78:81]
	v_mfma_f32_16x16x32_bf16 v[110:113], v[146:149], v[162:165], v[110:113]
	v_mfma_f32_16x16x32_bf16 v[106:109], v[154:157], v[162:165], v[106:109]
	v_mfma_f32_16x16x32_bf16 v[102:105], v[146:149], v[170:173], v[102:105]
	v_mfma_f32_16x16x32_bf16 v[98:101], v[154:157], v[170:173], v[98:101]
	v_mfma_f32_16x16x32_bf16 v[82:85], v[146:149], v[178:181], v[82:85]
	v_mfma_f32_16x16x32_bf16 v[74:77], v[154:157], v[178:181], v[74:77]
	v_mfma_f32_16x16x32_bf16 v[70:73], v[146:149], v[186:189], v[70:73]
	v_mfma_f32_16x16x32_bf16 v[66:69], v[154:157], v[186:189], v[66:69]
	v_mfma_f32_16x16x32_bf16 v[110:113], v[150:153], v[166:169], v[110:113]
	v_mfma_f32_16x16x32_bf16 v[106:109], v[158:161], v[166:169], v[106:109]
	v_mfma_f32_16x16x32_bf16 v[102:105], v[150:153], v[174:177], v[102:105]
	v_mfma_f32_16x16x32_bf16 v[98:101], v[158:161], v[174:177], v[98:101]
	v_mfma_f32_16x16x32_bf16 v[82:85], v[150:153], v[182:185], v[82:85]
	v_mfma_f32_16x16x32_bf16 v[74:77], v[158:161], v[182:185], v[74:77]
	v_mfma_f32_16x16x32_bf16 v[70:73], v[150:153], v[190:193], v[70:73]
	v_mfma_f32_16x16x32_bf16 v[66:69], v[158:161], v[190:193], v[66:69]
	s_setprio 0
	s_barrier
	ds_read_b128 v[162:165], v211 offset:49152
	ds_read_b128 v[166:169], v211 offset:50176
	ds_read_b128 v[170:173], v211 offset:51200
	ds_read_b128 v[174:177], v211 offset:52224
	ds_read_b128 v[178:181], v211 offset:53248
	ds_read_b128 v[182:185], v211 offset:54272
	ds_read_b128 v[186:189], v211 offset:55296
	ds_read_b128 v[190:193], v211 offset:56320
	s_mov_b32 m0, s33
	s_nop 0
	global_load_lds_dwordx4 v196, s[20:21]
	s_add_u32 s16, s16, 0x80080
	s_mov_b32 m0, s39
	s_nop 0
	global_load_lds_dwordx4 v197, s[20:21]
	s_addc_u32 s17, s17, 0
	s_mov_b32 m0, s42
	s_nop 0
	global_load_lds_dwordx4 v196, s[16:17]
	s_nop 0
	s_mov_b32 m0, s43
	s_nop 0
	global_load_lds_dwordx4 v197, s[16:17]
	s_add_u32 s16, s22, 0x80
	s_addc_u32 s17, s23, 0
	s_mov_b32 m0, s40
	s_nop 0
	global_load_lds_dwordx4 v202, s[16:17]
	s_nop 0
	s_mov_b32 m0, s41
	s_nop 0
	global_load_lds_dwordx4 v204, s[16:17]
	s_waitcnt vmcnt(8)
	s_waitcnt lgkmcnt(0)
	s_barrier
	s_setprio 1
	v_mfma_f32_16x16x32_bf16 v[62:65], v[130:133], v[162:165], v[62:65]
	v_mfma_f32_16x16x32_bf16 v[58:61], v[138:141], v[162:165], v[58:61]
	v_mfma_f32_16x16x32_bf16 v[54:57], v[130:133], v[170:173], v[54:57]
	v_mfma_f32_16x16x32_bf16 v[46:49], v[138:141], v[170:173], v[46:49]
	v_mfma_f32_16x16x32_bf16 v[38:41], v[130:133], v[178:181], v[38:41]
	v_mfma_f32_16x16x32_bf16 v[30:33], v[138:141], v[178:181], v[30:33]
	v_mfma_f32_16x16x32_bf16 v[22:25], v[130:133], v[186:189], v[22:25]
	v_mfma_f32_16x16x32_bf16 v[14:17], v[138:141], v[186:189], v[14:17]
	v_mfma_f32_16x16x32_bf16 v[62:65], v[134:137], v[166:169], v[62:65]
	v_mfma_f32_16x16x32_bf16 v[58:61], v[142:145], v[166:169], v[58:61]
	v_mfma_f32_16x16x32_bf16 v[54:57], v[134:137], v[174:177], v[54:57]
	v_mfma_f32_16x16x32_bf16 v[46:49], v[142:145], v[174:177], v[46:49]
	v_mfma_f32_16x16x32_bf16 v[38:41], v[134:137], v[182:185], v[38:41]
	v_mfma_f32_16x16x32_bf16 v[30:33], v[142:145], v[182:185], v[30:33]
	v_mfma_f32_16x16x32_bf16 v[22:25], v[134:137], v[190:193], v[22:25]
	v_mfma_f32_16x16x32_bf16 v[14:17], v[142:145], v[190:193], v[14:17]
	v_mfma_f32_16x16x32_bf16 v[50:53], v[146:149], v[162:165], v[50:53]
	v_mfma_f32_16x16x32_bf16 v[42:45], v[154:157], v[162:165], v[42:45]
	v_mfma_f32_16x16x32_bf16 v[34:37], v[146:149], v[170:173], v[34:37]
	v_mfma_f32_16x16x32_bf16 v[26:29], v[154:157], v[170:173], v[26:29]
	v_mfma_f32_16x16x32_bf16 v[18:21], v[146:149], v[178:181], v[18:21]
	v_mfma_f32_16x16x32_bf16 v[10:13], v[154:157], v[178:181], v[10:13]
	v_mfma_f32_16x16x32_bf16 v[6:9], v[146:149], v[186:189], v[6:9]
	v_mfma_f32_16x16x32_bf16 v[2:5], v[154:157], v[186:189], v[2:5]
	v_mfma_f32_16x16x32_bf16 v[50:53], v[150:153], v[166:169], v[50:53]
	v_mfma_f32_16x16x32_bf16 v[42:45], v[158:161], v[166:169], v[42:45]
	v_mfma_f32_16x16x32_bf16 v[34:37], v[150:153], v[174:177], v[34:37]
	v_mfma_f32_16x16x32_bf16 v[26:29], v[158:161], v[174:177], v[26:29]
	v_mfma_f32_16x16x32_bf16 v[18:21], v[150:153], v[182:185], v[18:21]
	v_mfma_f32_16x16x32_bf16 v[10:13], v[158:161], v[182:185], v[10:13]
	v_mfma_f32_16x16x32_bf16 v[6:9], v[150:153], v[190:193], v[6:9]
	v_mfma_f32_16x16x32_bf16 v[2:5], v[158:161], v[190:193], v[2:5]
	s_setprio 0
	s_barrier
	s_add_i32 s52, s52, 2
	s_cmp_gt_u32 s52, 29
	s_cbranch_scc1 .LBB0_987
	s_mov_b64 s[16:17], s[18:19]
	s_branch .LBB0_995

;     ...
;         if (Epi::NST > 0 && ui > 0) { PG_KPAIR(0, 8 + Epi::NST); t0 = 2; }
.LBB0_1995:
	s_cmp_lt_i32 s88, 1
	v_add_u32_e32 v51, 0x10000, v226
	v_add_u32_e32 v52, 0x14000, v226
	v_add_u32_e32 v53, 0x18000, v226
	v_add_u32_e32 v229, 0x1c000, v226
	s_cbranch_scc1 .LBB0_1997
	ds_read_b128 v[2:5], v51
	ds_read_b128 v[6:9], v51 offset:1024
	ds_read_b128 v[10:13], v51 offset:2048
	ds_read_b128 v[14:17], v51 offset:3072
	ds_read_b128 v[18:21], v52
	ds_read_b128 v[22:25], v52 offset:1024
	ds_read_b128 v[26:29], v52 offset:2048
	ds_read_b128 v[30:33], v52 offset:3072
	s_add_u32 s26, s6, 0x100
	s_addc_u32 s27, s7, 0
	ds_read_b128 v[34:37], v227
	ds_read_b128 v[38:41], v227 offset:1024
	ds_read_b128 v[42:45], v227 offset:2048
	ds_read_b128 v[46:49], v227 offset:3072
	ds_read_b128 v[182:185], v227 offset:4096
	ds_read_b128 v[186:189], v227 offset:5120
	ds_read_b128 v[190:193], v227 offset:6144
	ds_read_b128 v[194:197], v227 offset:7168
	s_mov_b32 m0, s62
	s_nop 0
	global_load_lds_dwordx4 v220, s[8:9]
	s_nop 0
	s_mov_b32 m0, s63
	s_nop 0
	global_load_lds_dwordx4 v222, s[8:9]
	s_waitcnt vmcnt(16)
	s_waitcnt lgkmcnt(0)
	s_barrier
	s_setprio 1
	v_mfma_scale_f32_16x16x128_f8f6f4 v[178:181], v[2:7], v[34:39], v[178:181], v8, v40 op_sel_hi:[0,0,0] cbsz:2 blgp:2
	v_mfma_scale_f32_16x16x128_f8f6f4 v[174:177], v[10:15], v[34:39], v[174:177], v16, v40 op_sel_hi:[0,0,0] cbsz:2 blgp:2
	v_mfma_scale_f32_16x16x128_f8f6f4 v[170:173], v[2:7], v[42:47], v[170:173], v8, v48 op_sel_hi:[0,0,0] cbsz:2 blgp:2
	v_mfma_scale_f32_16x16x128_f8f6f4 v[166:169], v[10:15], v[42:47], v[166:169], v16, v48 op_sel_hi:[0,0,0] cbsz:2 blgp:2
	v_mfma_scale_f32_16x16x128_f8f6f4 v[162:165], v[2:7], v[182:187], v[162:165], v8, v188 op_sel_hi:[0,0,0] cbsz:2 blgp:2
	v_mfma_scale_f32_16x16x128_f8f6f4 v[158:161], v[10:15], v[182:187], v[158:161], v16, v188 op_sel_hi:[0,0,0] cbsz:2 blgp:2
	v_mfma_scale_f32_16x16x128_f8f6f4 v[154:157], v[2:7], v[190:195], v[154:157], v8, v196 op_sel_hi:[0,0,0] cbsz:2 blgp:2
	v_mfma_scale_f32_16x16x128_f8f6f4 v[150:153], v[10:15], v[190:195], v[150:153], v16, v196 op_sel_hi:[0,0,0] cbsz:2 blgp:2
	v_mfma_scale_f32_16x16x128_f8f6f4 v[146:149], v[18:23], v[34:39], v[146:149], v24, v40 op_sel_hi:[0,0,0] cbsz:2 blgp:2
	v_mfma_scale_f32_16x16x128_f8f6f4 v[142:145], v[26:31], v[34:39], v[142:145], v32, v40 op_sel_hi:[0,0,0] cbsz:2 blgp:2
	v_mfma_scale_f32_16x16x128_f8f6f4 v[138:141], v[18:23], v[42:47], v[138:141], v24, v48 op_sel_hi:[0,0,0] cbsz:2 blgp:2
	v_mfma_scale_f32_16x16x128_f8f6f4 v[134:137], v[26:31], v[42:47], v[134:137], v32, v48 op_sel_hi:[0,0,0] cbsz:2 blgp:2
	v_mfma_scale_f32_16x16x128_f8f6f4 v[130:133], v[18:23], v[182:187], v[130:133], v24, v188 op_sel_hi:[0,0,0] cbsz:2 blgp:2
	v_mfma_scale_f32_16x16x128_f8f6f4 v[126:129], v[26:31], v[182:187], v[126:129], v32, v188 op_sel_hi:[0,0,0] cbsz:2 blgp:2
	v_mfma_scale_f32_16x16x128_f8f6f4 v[122:125], v[18:23], v[190:195], v[122:125], v24, v196 op_sel_hi:[0,0,0] cbsz:2 blgp:2
	v_mfma_scale_f32_16x16x128_f8f6f4 v[118:121], v[26:31], v[190:195], v[118:121], v32, v196 op_sel_hi:[0,0,0] cbsz:2 blgp:2
	s_setprio 0
	s_barrier
	ds_read_b128 v[34:37], v227 offset:16384
	ds_read_b128 v[38:41], v227 offset:17408
	ds_read_b128 v[42:45], v227 offset:18432
	ds_read_b128 v[46:49], v227 offset:19456
	ds_read_b128 v[182:185], v227 offset:20480
	ds_read_b128 v[186:189], v227 offset:21504
	ds_read_b128 v[190:193], v227 offset:22528
	ds_read_b128 v[194:197], v227 offset:23552
	s_mov_b32 m0, s47
	s_nop 0
	global_load_lds_dwordx4 v219, s[10:11]
	s_nop 0
	s_mov_b32 m0, s53
	s_nop 0
	global_load_lds_dwordx4 v221, s[10:11]
	s_waitcnt vmcnt(12)
	s_waitcnt lgkmcnt(0)
	s_barrier
	s_setprio 1
	v_mfma_scale_f32_16x16x128_f8f6f4 v[114:117], v[2:7], v[34:39], v[114:117], v8, v40 op_sel_hi:[0,0,0] cbsz:2 blgp:2
	v_mfma_scale_f32_16x16x128_f8f6f4 v[110:113], v[10:15], v[34:39], v[110:113], v16, v40 op_sel_hi:[0,0,0] cbsz:2 blgp:2
	s_mov_b32 m0, s48
	s_nop 0
	global_load_lds_dwordx4 v214, s[26:27]
	v_mfma_scale_f32_16x16x128_f8f6f4 v[106:109], v[2:7], v[42:47], v[106:109], v8, v48 op_sel_hi:[0,0,0] cbsz:2 blgp:2
	v_mfma_scale_f32_16x16x128_f8f6f4 v[102:105], v[10:15], v[42:47], v[102:105], v16, v48 op_sel_hi:[0,0,0] cbsz:2 blgp:2
	s_mov_b32 m0, s49
	s_nop 0
	global_load_lds_dwordx4 v215, s[26:27]
	s_add_u32 s26, s6, 0x40100
	s_addc_u32 s27, s7, 0
	v_mfma_scale_f32_16x16x128_f8f6f4 v[98:101], v[2:7], v[182:187], v[98:101], v8, v188 op_sel_hi:[0,0,0] cbsz:2 blgp:2
	v_mfma_scale_f32_16x16x128_f8f6f4 v[94:97], v[10:15], v[182:187], v[94:97], v16, v188 op_sel_hi:[0,0,0] cbsz:2 blgp:2
	v_mfma_scale_f32_16x16x128_f8f6f4 v[90:93], v[2:7], v[190:195], v[90:93], v8, v196 op_sel_hi:[0,0,0] cbsz:2 blgp:2
	v_mfma_scale_f32_16x16x128_f8f6f4 v[86:89], v[10:15], v[190:195], v[86:89], v16, v196 op_sel_hi:[0,0,0] cbsz:2 blgp:2
	v_mfma_scale_f32_16x16x128_f8f6f4 v[82:85], v[18:23], v[34:39], v[82:85], v24, v40 op_sel_hi:[0,0,0] cbsz:2 blgp:2
	v_mfma_scale_f32_16x16x128_f8f6f4 v[78:81], v[26:31], v[34:39], v[78:81], v32, v40 op_sel_hi:[0,0,0] cbsz:2 blgp:2
	s_mov_b32 m0, s51
	s_nop 0
	global_load_lds_dwordx4 v214, s[26:27]
	v_mfma_scale_f32_16x16x128_f8f6f4 v[74:77], v[18:23], v[42:47], v[74:77], v24, v48 op_sel_hi:[0,0,0] cbsz:2 blgp:2
	v_mfma_scale_f32_16x16x128_f8f6f4 v[70:73], v[26:31], v[42:47], v[70:73], v32, v48 op_sel_hi:[0,0,0] cbsz:2 blgp:2
	s_mov_b32 m0, s52
	s_nop 0
	global_load_lds_dwordx4 v215, s[26:27]
	v_mfma_scale_f32_16x16x128_f8f6f4 v[66:69], v[18:23], v[182:187], v[66:69], v24, v188 op_sel_hi:[0,0,0] cbsz:2 blgp:2
	v_mfma_scale_f32_16x16x128_f8f6f4 v[62:65], v[26:31], v[182:187], v[62:65], v32, v188 op_sel_hi:[0,0,0] cbsz:2 blgp:2
	v_mfma_scale_f32_16x16x128_f8f6f4 v[58:61], v[18:23], v[190:195], v[58:61], v24, v196 op_sel_hi:[0,0,0] cbsz:2 blgp:2
	v_mfma_scale_f32_16x16x128_f8f6f4 v[54:57], v[26:31], v[190:195], v[54:57], v32, v196 op_sel_hi:[0,0,0] cbsz:2 blgp:2
	s_setprio 0
	s_barrier
	ds_read_b128 v[2:5], v53
	ds_read_b128 v[6:9], v53 offset:1024
	ds_read_b128 v[10:13], v53 offset:2048
	ds_read_b128 v[14:17], v53 offset:3072
	ds_read_b128 v[18:21], v229
	ds_read_b128 v[22:25], v229 offset:1024
	ds_read_b128 v[26:29], v229 offset:2048
	ds_read_b128 v[30:33], v229 offset:3072
	ds_read_b128 v[34:37], v227 offset:32768
	ds_read_b128 v[38:41], v227 offset:33792
	ds_read_b128 v[42:45], v227 offset:34816
	ds_read_b128 v[46:49], v227 offset:35840
	ds_read_b128 v[182:185], v227 offset:36864
	ds_read_b128 v[186:189], v227 offset:37888
	ds_read_b128 v[190:193], v227 offset:38912
	ds_read_b128 v[194:197], v227 offset:39936
	s_mov_b32 m0, s54
	s_nop 0
	global_load_lds_dwordx4 v220, s[10:11]
	s_nop 0
	s_mov_b32 m0, s55
	s_nop 0
	global_load_lds_dwordx4 v222, s[10:11]
	s_waitcnt vmcnt(8)
	s_waitcnt lgkmcnt(0)
	s_barrier
	s_setprio 1
	v_mfma_scale_f32_16x16x128_f8f6f4 v[178:181], v[2:7], v[34:39], v[178:181], v8, v40 op_sel_hi:[0,0,0] cbsz:2 blgp:2
	v_mfma_scale_f32_16x16x128_f8f6f4 v[174:177], v[10:15], v[34:39], v[174:177], v16, v40 op_sel_hi:[0,0,0] cbsz:2 blgp:2
	v_mfma_scale_f32_16x16x128_f8f6f4 v[170:173], v[2:7], v[42:47], v[170:173], v8, v48 op_sel_hi:[0,0,0] cbsz:2 blgp:2
	v_mfma_scale_f32_16x16x128_f8f6f4 v[166:169], v[10:15], v[42:47], v[166:169], v16, v48 op_sel_hi:[0,0,0] cbsz:2 blgp:2
	v_mfma_scale_f32_16x16x128_f8f6f4 v[162:165], v[2:7], v[182:187], v[162:165], v8, v188 op_sel_hi:[0,0,0] cbsz:2 blgp:2
	v_mfma_scale_f32_16x16x128_f8f6f4 v[158:161], v[10:15], v[182:187], v[158:161], v16, v188 op_sel_hi:[0,0,0] cbsz:2 blgp:2
	v_mfma_scale_f32_16x16x128_f8f6f4 v[154:157], v[2:7], v[190:195], v[154:157], v8, v196 op_sel_hi:[0,0,0] cbsz:2 blgp:2
	v_mfma_scale_f32_16x16x128_f8f6f4 v[150:153], v[10:15], v[190:195], v[150:153], v16, v196 op_sel_hi:[0,0,0] cbsz:2 blgp:2
	v_mfma_scale_f32_16x16x128_f8f6f4 v[146:149], v[18:23], v[34:39], v[146:149], v24, v40 op_sel_hi:[0,0,0] cbsz:2 blgp:2
	v_mfma_scale_f32_16x16x128_f8f6f4 v[142:145], v[26:31], v[34:39], v[142:145], v32, v40 op_sel_hi:[0,0,0] cbsz:2 blgp:2
	v_mfma_scale_f32_16x16x128_f8f6f4 v[138:141], v[18:23], v[42:47], v[138:141], v24, v48 op_sel_hi:[0,0,0] cbsz:2 blgp:2
	v_mfma_scale_f32_16x16x128_f8f6f4 v[134:137], v[26:31], v[42:47], v[134:137], v32, v48 op_sel_hi:[0,0,0] cbsz:2 blgp:2
	v_mfma_scale_f32_16x16x128_f8f6f4 v[130:133], v[18:23], v[182:187], v[130:133], v24, v188 op_sel_hi:[0,0,0] cbsz:2 blgp:2
	v_mfma_scale_f32_16x16x128_f8f6f4 v[126:129], v[26:31], v[182:187], v[126:129], v32, v188 op_sel_hi:[0,0,0] cbsz:2 blgp:2
	v_mfma_scale_f32_16x16x128_f8f6f4 v[122:125], v[18:23], v[190:195], v[122:125], v24, v196 op_sel_hi:[0,0,0] cbsz:2 blgp:2
	v_mfma_scale_f32_16x16x128_f8f6f4 v[118:121], v[26:31], v[190:195], v[118:121], v32, v196 op_sel_hi:[0,0,0] cbsz:2 blgp:2
	s_setprio 0
	s_barrier
	ds_read_b128 v[34:37], v227 offset:49152
	ds_read_b128 v[38:41], v227 offset:50176
	ds_read_b128 v[42:45], v227 offset:51200
	ds_read_b128 v[46:49], v227 offset:52224
	ds_read_b128 v[182:185], v227 offset:53248
	ds_read_b128 v[186:189], v227 offset:54272
	ds_read_b128 v[190:193], v227 offset:55296
	ds_read_b128 v[194:197], v227 offset:56320
	s_mov_b32 m0, s58
	s_nop 0
	global_load_lds_dwordx4 v219, s[12:13]
	s_nop 0
	s_mov_b32 m0, s59
	s_nop 0
	global_load_lds_dwordx4 v221, s[12:13]
	s_waitcnt vmcnt(4)
	s_waitcnt lgkmcnt(0)
	s_barrier
	s_setprio 1
	s_add_u32 s26, s6, 0x180
	s_addc_u32 s27, s7, 0
	v_mfma_scale_f32_16x16x128_f8f6f4 v[114:117], v[2:7], v[34:39], v[114:117], v8, v40 op_sel_hi:[0,0,0] cbsz:2 blgp:2
	v_mfma_scale_f32_16x16x128_f8f6f4 v[110:113], v[10:15], v[34:39], v[110:113], v16, v40 op_sel_hi:[0,0,0] cbsz:2 blgp:2
	s_mov_b32 m0, s56
	s_nop 0
	global_load_lds_dwordx4 v214, s[26:27]
	v_mfma_scale_f32_16x16x128_f8f6f4 v[106:109], v[2:7], v[42:47], v[106:109], v8, v48 op_sel_hi:[0,0,0] cbsz:2 blgp:2
	v_mfma_scale_f32_16x16x128_f8f6f4 v[102:105], v[10:15], v[42:47], v[102:105], v16, v48 op_sel_hi:[0,0,0] cbsz:2 blgp:2
	s_mov_b32 m0, s57
	s_nop 0
	global_load_lds_dwordx4 v215, s[26:27]
	s_add_u32 s26, s6, 0x40180
	s_addc_u32 s27, s7, 0
	v_mfma_scale_f32_16x16x128_f8f6f4 v[98:101], v[2:7], v[182:187], v[98:101], v8, v188 op_sel_hi:[0,0,0] cbsz:2 blgp:2
	v_mfma_scale_f32_16x16x128_f8f6f4 v[94:97], v[10:15], v[182:187], v[94:97], v16, v188 op_sel_hi:[0,0,0] cbsz:2 blgp:2
	v_mfma_scale_f32_16x16x128_f8f6f4 v[90:93], v[2:7], v[190:195], v[90:93], v8, v196 op_sel_hi:[0,0,0] cbsz:2 blgp:2
	v_mfma_scale_f32_16x16x128_f8f6f4 v[86:89], v[10:15], v[190:195], v[86:89], v16, v196 op_sel_hi:[0,0,0] cbsz:2 blgp:2
	v_mfma_scale_f32_16x16x128_f8f6f4 v[82:85], v[18:23], v[34:39], v[82:85], v24, v40 op_sel_hi:[0,0,0] cbsz:2 blgp:2
	v_mfma_scale_f32_16x16x128_f8f6f4 v[78:81], v[26:31], v[34:39], v[78:81], v32, v40 op_sel_hi:[0,0,0] cbsz:2 blgp:2
	s_mov_b32 m0, s60
	s_nop 0
	global_load_lds_dwordx4 v214, s[26:27]
	v_mfma_scale_f32_16x16x128_f8f6f4 v[74:77], v[18:23], v[42:47], v[74:77], v24, v48 op_sel_hi:[0,0,0] cbsz:2 blgp:2
	v_mfma_scale_f32_16x16x128_f8f6f4 v[70:73], v[26:31], v[42:47], v[70:73], v32, v48 op_sel_hi:[0,0,0] cbsz:2 blgp:2
	s_mov_b32 m0, s61
	s_nop 0
	global_load_lds_dwordx4 v215, s[26:27]
	v_mfma_scale_f32_16x16x128_f8f6f4 v[66:69], v[18:23], v[182:187], v[66:69], v24, v188 op_sel_hi:[0,0,0] cbsz:2 blgp:2
	v_mfma_scale_f32_16x16x128_f8f6f4 v[62:65], v[26:31], v[182:187], v[62:65], v32, v188 op_sel_hi:[0,0,0] cbsz:2 blgp:2
	v_mfma_scale_f32_16x16x128_f8f6f4 v[58:61], v[18:23], v[190:195], v[58:61], v24, v196 op_sel_hi:[0,0,0] cbsz:2 blgp:2
	v_mfma_scale_f32_16x16x128_f8f6f4 v[54:57], v[26:31], v[190:195], v[54:57], v32, v196 op_sel_hi:[0,0,0] cbsz:2 blgp:2
	s_setprio 0
	s_barrier
	s_mov_b32 s28, 2
	s_branch .LBB0_1998

.LBB0_1999:
	s_add_i32 s38, s36, 0xe08c0100
	s_and_b64 s[36:37], s[34:35], exec
	s_cselect_b32 s77, s38, 0
	s_add_u32 s36, s41, s40
	s_addc_u32 s37, s76, 0
	s_waitcnt vmcnt(8)
	s_and_b64 s[34:35], s[34:35], exec
	s_waitcnt lgkmcnt(0)
	s_cselect_b32 s34, s36, s23
	s_cselect_b32 s35, s37, s2
	s_add_u32 s36, s34, 0x80
	s_addc_u32 s37, s35, 0
	s_barrier
	s_setprio 1
	v_mfma_scale_f32_16x16x128_f8f6f4 v[178:181], v[18:23], v[190:195], v[178:181], v24, v196 op_sel_hi:[0,0,0] cbsz:2 blgp:2
	v_mfma_scale_f32_16x16x128_f8f6f4 v[174:177], v[26:31], v[190:195], v[174:177], v32, v196 op_sel_hi:[0,0,0] cbsz:2 blgp:2
	v_mfma_scale_f32_16x16x128_f8f6f4 v[170:173], v[18:23], v[182:187], v[170:173], v24, v188 op_sel_hi:[0,0,0] cbsz:2 blgp:2
	v_mfma_scale_f32_16x16x128_f8f6f4 v[166:169], v[26:31], v[182:187], v[166:169], v32, v188 op_sel_hi:[0,0,0] cbsz:2 blgp:2
	v_mfma_scale_f32_16x16x128_f8f6f4 v[162:165], v[18:23], v[42:47], v[162:165], v24, v48 op_sel_hi:[0,0,0] cbsz:2 blgp:2
	v_mfma_scale_f32_16x16x128_f8f6f4 v[158:161], v[26:31], v[42:47], v[158:161], v32, v48 op_sel_hi:[0,0,0] cbsz:2 blgp:2
	v_mfma_scale_f32_16x16x128_f8f6f4 v[154:157], v[18:23], v[34:39], v[154:157], v24, v40 op_sel_hi:[0,0,0] cbsz:2 blgp:2
	v_mfma_scale_f32_16x16x128_f8f6f4 v[150:153], v[26:31], v[34:39], v[150:153], v32, v40 op_sel_hi:[0,0,0] cbsz:2 blgp:2
	v_mfma_scale_f32_16x16x128_f8f6f4 v[146:149], v[2:7], v[190:195], v[146:149], v8, v196 op_sel_hi:[0,0,0] cbsz:2 blgp:2
	v_mfma_scale_f32_16x16x128_f8f6f4 v[142:145], v[10:15], v[190:195], v[142:145], v16, v196 op_sel_hi:[0,0,0] cbsz:2 blgp:2
	v_mfma_scale_f32_16x16x128_f8f6f4 v[138:141], v[2:7], v[182:187], v[138:141], v8, v188 op_sel_hi:[0,0,0] cbsz:2 blgp:2
	v_mfma_scale_f32_16x16x128_f8f6f4 v[134:137], v[10:15], v[182:187], v[134:137], v16, v188 op_sel_hi:[0,0,0] cbsz:2 blgp:2
	v_mfma_scale_f32_16x16x128_f8f6f4 v[130:133], v[2:7], v[42:47], v[130:133], v8, v48 op_sel_hi:[0,0,0] cbsz:2 blgp:2
	v_mfma_scale_f32_16x16x128_f8f6f4 v[126:129], v[10:15], v[42:47], v[126:129], v16, v48 op_sel_hi:[0,0,0] cbsz:2 blgp:2
	v_mfma_scale_f32_16x16x128_f8f6f4 v[122:125], v[2:7], v[34:39], v[122:125], v8, v40 op_sel_hi:[0,0,0] cbsz:2 blgp:2
	v_mfma_scale_f32_16x16x128_f8f6f4 v[118:121], v[10:15], v[34:39], v[118:121], v16, v40 op_sel_hi:[0,0,0] cbsz:2 blgp:2
	s_setprio 0
	s_barrier
	ds_read_b128 v[34:37], v227 offset:16384
	ds_read_b128 v[38:41], v227 offset:17408
	ds_read_b128 v[42:45], v227 offset:18432
	ds_read_b128 v[46:49], v227 offset:19456
	ds_read_b128 v[182:185], v227 offset:20480
	ds_read_b128 v[186:189], v227 offset:21504
	ds_read_b128 v[190:193], v227 offset:22528
	ds_read_b128 v[194:197], v227 offset:23552
	s_add_u32 s38, s4, s77
	s_addc_u32 s39, s5, 0
	s_mov_b32 m0, s47
	s_nop 0
	global_load_lds_dwordx4 v219, s[38:39]
	s_nop 0
	s_mov_b32 m0, s53
	s_nop 0
	global_load_lds_dwordx4 v221, s[38:39]
	s_waitcnt vmcnt(4)
	s_waitcnt lgkmcnt(0)
	s_barrier
	s_setprio 1
	v_mfma_scale_f32_16x16x128_f8f6f4 v[114:117], v[18:23], v[34:39], v[114:117], v24, v40 op_sel_hi:[0,0,0] cbsz:2 blgp:2
	v_mfma_scale_f32_16x16x128_f8f6f4 v[110:113], v[26:31], v[34:39], v[110:113], v32, v40 op_sel_hi:[0,0,0] cbsz:2 blgp:2
	s_mov_b32 m0, s48
	s_nop 0
	global_load_lds_dwordx4 v214, s[34:35]
	v_mfma_scale_f32_16x16x128_f8f6f4 v[106:109], v[18:23], v[42:47], v[106:109], v24, v48 op_sel_hi:[0,0,0] cbsz:2 blgp:2
	v_mfma_scale_f32_16x16x128_f8f6f4 v[102:105], v[26:31], v[42:47], v[102:105], v32, v48 op_sel_hi:[0,0,0] cbsz:2 blgp:2
	s_add_u32 s100, s34, 0x40000
	s_addc_u32 s101, s35, 0
	s_mov_b32 m0, s49
	s_nop 0
	global_load_lds_dwordx4 v215, s[34:35]
	v_mfma_scale_f32_16x16x128_f8f6f4 v[98:101], v[18:23], v[182:187], v[98:101], v24, v188 op_sel_hi:[0,0,0] cbsz:2 blgp:2
	v_mfma_scale_f32_16x16x128_f8f6f4 v[94:97], v[26:31], v[182:187], v[94:97], v32, v188 op_sel_hi:[0,0,0] cbsz:2 blgp:2
	v_mfma_scale_f32_16x16x128_f8f6f4 v[90:93], v[18:23], v[190:195], v[90:93], v24, v196 op_sel_hi:[0,0,0] cbsz:2 blgp:2
	v_mfma_scale_f32_16x16x128_f8f6f4 v[86:89], v[26:31], v[190:195], v[86:89], v32, v196 op_sel_hi:[0,0,0] cbsz:2 blgp:2
	v_mfma_scale_f32_16x16x128_f8f6f4 v[82:85], v[2:7], v[34:39], v[82:85], v8, v40 op_sel_hi:[0,0,0] cbsz:2 blgp:2
	v_mfma_scale_f32_16x16x128_f8f6f4 v[78:81], v[10:15], v[34:39], v[78:81], v16, v40 op_sel_hi:[0,0,0] cbsz:2 blgp:2
	s_mov_b32 m0, s51
	s_nop 0
	global_load_lds_dwordx4 v214, s[100:101]
	v_mfma_scale_f32_16x16x128_f8f6f4 v[74:77], v[2:7], v[42:47], v[74:77], v8, v48 op_sel_hi:[0,0,0] cbsz:2 blgp:2
	v_mfma_scale_f32_16x16x128_f8f6f4 v[70:73], v[10:15], v[42:47], v[70:73], v16, v48 op_sel_hi:[0,0,0] cbsz:2 blgp:2
	s_mov_b32 m0, s52
	s_nop 0
	global_load_lds_dwordx4 v215, s[100:101]
	v_mfma_scale_f32_16x16x128_f8f6f4 v[66:69], v[2:7], v[182:187], v[66:69], v8, v188 op_sel_hi:[0,0,0] cbsz:2 blgp:2
	v_mfma_scale_f32_16x16x128_f8f6f4 v[62:65], v[10:15], v[182:187], v[62:65], v16, v188 op_sel_hi:[0,0,0] cbsz:2 blgp:2
	v_mfma_scale_f32_16x16x128_f8f6f4 v[58:61], v[2:7], v[190:195], v[58:61], v8, v196 op_sel_hi:[0,0,0] cbsz:2 blgp:2
	v_mfma_scale_f32_16x16x128_f8f6f4 v[54:57], v[10:15], v[190:195], v[54:57], v16, v196 op_sel_hi:[0,0,0] cbsz:2 blgp:2
	s_setprio 0
	s_barrier
	ds_read_b128 v[2:5], v53
	ds_read_b128 v[6:9], v53 offset:1024
	ds_read_b128 v[10:13], v53 offset:2048
	ds_read_b128 v[14:17], v53 offset:3072
	ds_read_b128 v[18:21], v229
	ds_read_b128 v[22:25], v229 offset:1024
	ds_read_b128 v[26:29], v229 offset:2048
	ds_read_b128 v[30:33], v229 offset:3072
	ds_read_b128 v[34:37], v227 offset:32768
	ds_read_b128 v[38:41], v227 offset:33792
	ds_read_b128 v[42:45], v227 offset:34816
	ds_read_b128 v[46:49], v227 offset:35840
	ds_read_b128 v[182:185], v227 offset:36864
	ds_read_b128 v[186:189], v227 offset:37888
	ds_read_b128 v[190:193], v227 offset:38912
	ds_read_b128 v[194:197], v227 offset:39936
	s_mov_b32 m0, s54
	s_nop 0
	global_load_lds_dwordx4 v220, s[38:39]
	s_nop 0
	s_mov_b32 m0, s55
	s_nop 0
	global_load_lds_dwordx4 v222, s[38:39]
	s_waitcnt vmcnt(8)
	s_waitcnt lgkmcnt(0)
	s_barrier
	s_setprio 1
	v_mfma_scale_f32_16x16x128_f8f6f4 v[178:181], v[2:7], v[34:39], v[178:181], v8, v40 op_sel_hi:[0,0,0] cbsz:2 blgp:2
	v_mfma_scale_f32_16x16x128_f8f6f4 v[174:177], v[10:15], v[34:39], v[174:177], v16, v40 op_sel_hi:[0,0,0] cbsz:2 blgp:2
	v_mfma_scale_f32_16x16x128_f8f6f4 v[170:173], v[2:7], v[42:47], v[170:173], v8, v48 op_sel_hi:[0,0,0] cbsz:2 blgp:2
	v_mfma_scale_f32_16x16x128_f8f6f4 v[166:169], v[10:15], v[42:47], v[166:169], v16, v48 op_sel_hi:[0,0,0] cbsz:2 blgp:2
	v_mfma_scale_f32_16x16x128_f8f6f4 v[162:165], v[2:7], v[182:187], v[162:165], v8, v188 op_sel_hi:[0,0,0] cbsz:2 blgp:2
	v_mfma_scale_f32_16x16x128_f8f6f4 v[158:161], v[10:15], v[182:187], v[158:161], v16, v188 op_sel_hi:[0,0,0] cbsz:2 blgp:2
	v_mfma_scale_f32_16x16x128_f8f6f4 v[154:157], v[2:7], v[190:195], v[154:157], v8, v196 op_sel_hi:[0,0,0] cbsz:2 blgp:2
	v_mfma_scale_f32_16x16x128_f8f6f4 v[150:153], v[10:15], v[190:195], v[150:153], v16, v196 op_sel_hi:[0,0,0] cbsz:2 blgp:2
	v_mfma_scale_f32_16x16x128_f8f6f4 v[146:149], v[18:23], v[34:39], v[146:149], v24, v40 op_sel_hi:[0,0,0] cbsz:2 blgp:2
	v_mfma_scale_f32_16x16x128_f8f6f4 v[142:145], v[26:31], v[34:39], v[142:145], v32, v40 op_sel_hi:[0,0,0] cbsz:2 blgp:2
	v_mfma_scale_f32_16x16x128_f8f6f4 v[138:141], v[18:23], v[42:47], v[138:141], v24, v48 op_sel_hi:[0,0,0] cbsz:2 blgp:2
	v_mfma_scale_f32_16x16x128_f8f6f4 v[134:137], v[26:31], v[42:47], v[134:137], v32, v48 op_sel_hi:[0,0,0] cbsz:2 blgp:2
	v_mfma_scale_f32_16x16x128_f8f6f4 v[130:133], v[18:23], v[182:187], v[130:133], v24, v188 op_sel_hi:[0,0,0] cbsz:2 blgp:2
	v_mfma_scale_f32_16x16x128_f8f6f4 v[126:129], v[26:31], v[182:187], v[126:129], v32, v188 op_sel_hi:[0,0,0] cbsz:2 blgp:2
	v_mfma_scale_f32_16x16x128_f8f6f4 v[122:125], v[18:23], v[190:195], v[122:125], v24, v196 op_sel_hi:[0,0,0] cbsz:2 blgp:2
	v_mfma_scale_f32_16x16x128_f8f6f4 v[118:121], v[26:31], v[190:195], v[118:121], v32, v196 op_sel_hi:[0,0,0] cbsz:2 blgp:2
	s_setprio 0
	s_barrier
	ds_read_b128 v[34:37], v227 offset:49152
	ds_read_b128 v[38:41], v227 offset:50176
	ds_read_b128 v[42:45], v227 offset:51200
	ds_read_b128 v[46:49], v227 offset:52224
	ds_read_b128 v[182:185], v227 offset:53248
	ds_read_b128 v[186:189], v227 offset:54272
	ds_read_b128 v[190:193], v227 offset:55296
	ds_read_b128 v[194:197], v227 offset:56320
	s_add_u32 s100, s38, 0x80
	s_addc_u32 s101, s39, 0
	s_mov_b32 m0, s58
	s_nop 0
	global_load_lds_dwordx4 v219, s[100:101]
	s_nop 0
	s_mov_b32 m0, s59
	s_nop 0
	global_load_lds_dwordx4 v221, s[100:101]
	s_waitcnt vmcnt(4)
	s_waitcnt lgkmcnt(0)
	s_barrier
	s_setprio 1
	v_mfma_scale_f32_16x16x128_f8f6f4 v[114:117], v[2:7], v[34:39], v[114:117], v8, v40 op_sel_hi:[0,0,0] cbsz:2 blgp:2
	v_mfma_scale_f32_16x16x128_f8f6f4 v[110:113], v[10:15], v[34:39], v[110:113], v16, v40 op_sel_hi:[0,0,0] cbsz:2 blgp:2
	s_mov_b32 m0, s56
	s_nop 0
	global_load_lds_dwordx4 v214, s[36:37]
	v_mfma_scale_f32_16x16x128_f8f6f4 v[106:109], v[2:7], v[42:47], v[106:109], v8, v48 op_sel_hi:[0,0,0] cbsz:2 blgp:2
	v_mfma_scale_f32_16x16x128_f8f6f4 v[102:105], v[10:15], v[42:47], v[102:105], v16, v48 op_sel_hi:[0,0,0] cbsz:2 blgp:2
	s_mov_b32 m0, s57
	s_nop 0
	global_load_lds_dwordx4 v215, s[36:37]
	s_add_u32 s34, s34, 0x40080
	s_addc_u32 s35, s35, 0
	v_mfma_scale_f32_16x16x128_f8f6f4 v[98:101], v[2:7], v[182:187], v[98:101], v8, v188 op_sel_hi:[0,0,0] cbsz:2 blgp:2
	v_mfma_scale_f32_16x16x128_f8f6f4 v[94:97], v[10:15], v[182:187], v[94:97], v16, v188 op_sel_hi:[0,0,0] cbsz:2 blgp:2
	v_mfma_scale_f32_16x16x128_f8f6f4 v[90:93], v[2:7], v[190:195], v[90:93], v8, v196 op_sel_hi:[0,0,0] cbsz:2 blgp:2
	v_mfma_scale_f32_16x16x128_f8f6f4 v[86:89], v[10:15], v[190:195], v[86:89], v16, v196 op_sel_hi:[0,0,0] cbsz:2 blgp:2
	v_mfma_scale_f32_16x16x128_f8f6f4 v[82:85], v[18:23], v[34:39], v[82:85], v24, v40 op_sel_hi:[0,0,0] cbsz:2 blgp:2
	v_mfma_scale_f32_16x16x128_f8f6f4 v[78:81], v[26:31], v[34:39], v[78:81], v32, v40 op_sel_hi:[0,0,0] cbsz:2 blgp:2
	s_mov_b32 m0, s60
	s_nop 0
	global_load_lds_dwordx4 v214, s[34:35]
	v_mfma_scale_f32_16x16x128_f8f6f4 v[74:77], v[18:23], v[42:47], v[74:77], v24, v48 op_sel_hi:[0,0,0] cbsz:2 blgp:2
	v_mfma_scale_f32_16x16x128_f8f6f4 v[70:73], v[26:31], v[42:47], v[70:73], v32, v48 op_sel_hi:[0,0,0] cbsz:2 blgp:2
	s_mov_b32 m0, s61
	s_nop 0
	global_load_lds_dwordx4 v215, s[34:35]
	v_mfma_scale_f32_16x16x128_f8f6f4 v[66:69], v[18:23], v[182:187], v[66:69], v24, v188 op_sel_hi:[0,0,0] cbsz:2 blgp:2
	v_mfma_scale_f32_16x16x128_f8f6f4 v[62:65], v[26:31], v[182:187], v[62:65], v32, v188 op_sel_hi:[0,0,0] cbsz:2 blgp:2
	v_mfma_scale_f32_16x16x128_f8f6f4 v[58:61], v[18:23], v[190:195], v[58:61], v24, v196 op_sel_hi:[0,0,0] cbsz:2 blgp:2
	v_mfma_scale_f32_16x16x128_f8f6f4 v[54:57], v[26:31], v[190:195], v[54:57], v32, v196 op_sel_hi:[0,0,0] cbsz:2 blgp:2
	s_setprio 0
	s_barrier
	s_add_i32 s33, s33, 2
	s_add_u32 s41, s41, 0x100
	s_addc_u32 s76, s76, 0
	s_add_u32 s30, s30, 0x100
	s_addc_u32 s31, s31, 0
	s_add_u32 s28, s28, 0x100
	s_addc_u32 s29, s29, 0
	s_cmp_gt_u32 s33, 13
	s_cbranch_scc1 .LBB0_2002

;     ...
;         if (Epi::NST > 0 && ui > 0) { PG_KPAIR(0, 8 + Epi::NST); t0 = 2; }
.LBB0_2899:
	s_cmp_lt_i32 s93, 1
	v_add_u32_e32 v67, 0x10000, v212
	v_add_u32_e32 v68, 0x14000, v212
	v_add_u32_e32 v69, 0x18000, v212
	v_add_u32_e32 v215, 0x1c000, v212
	s_cbranch_scc1 .LBB0_2901
	ds_read_b128 v[2:5], v67
	ds_read_b128 v[6:9], v67 offset:1024
	ds_read_b128 v[10:13], v67 offset:2048
	ds_read_b128 v[14:17], v67 offset:3072
	ds_read_b128 v[18:21], v68
	ds_read_b128 v[22:25], v68 offset:1024
	ds_read_b128 v[26:29], v68 offset:2048
	ds_read_b128 v[30:33], v68 offset:3072
	s_add_u32 s30, s8, 0x100
	s_addc_u32 s31, s9, 0
	ds_read_b128 v[34:37], v213
	ds_read_b128 v[38:41], v213 offset:1024
	ds_read_b128 v[42:45], v213 offset:2048
	ds_read_b128 v[46:49], v213 offset:3072
	ds_read_b128 v[50:53], v213 offset:4096
	ds_read_b128 v[54:57], v213 offset:5120
	ds_read_b128 v[58:61], v213 offset:6144
	ds_read_b128 v[62:65], v213 offset:7168
	s_mov_b32 m0, s64
	s_nop 0
	global_load_lds_dwordx4 v204, s[10:11]
	s_nop 0
	s_mov_b32 m0, s65
	s_nop 0
	global_load_lds_dwordx4 v205, s[10:11]
	s_waitcnt vmcnt(24)
	s_waitcnt lgkmcnt(0)
	s_barrier
	s_setprio 1
	v_mfma_scale_f32_16x16x128_f8f6f4 v[194:197], v[2:9], v[34:41], v[194:197], v211, v211 op_sel_hi:[0,0,0]
	v_mfma_scale_f32_16x16x128_f8f6f4 v[190:193], v[10:17], v[34:41], v[190:193], v211, v211 op_sel_hi:[0,0,0]
	v_mfma_scale_f32_16x16x128_f8f6f4 v[186:189], v[2:9], v[42:49], v[186:189], v211, v211 op_sel_hi:[0,0,0]
	v_mfma_scale_f32_16x16x128_f8f6f4 v[182:185], v[10:17], v[42:49], v[182:185], v211, v211 op_sel_hi:[0,0,0]
	v_mfma_scale_f32_16x16x128_f8f6f4 v[178:181], v[2:9], v[50:57], v[178:181], v211, v211 op_sel_hi:[0,0,0]
	v_mfma_scale_f32_16x16x128_f8f6f4 v[174:177], v[10:17], v[50:57], v[174:177], v211, v211 op_sel_hi:[0,0,0]
	v_mfma_scale_f32_16x16x128_f8f6f4 v[170:173], v[2:9], v[58:65], v[170:173], v211, v211 op_sel_hi:[0,0,0]
	v_mfma_scale_f32_16x16x128_f8f6f4 v[166:169], v[10:17], v[58:65], v[166:169], v211, v211 op_sel_hi:[0,0,0]
	v_mfma_scale_f32_16x16x128_f8f6f4 v[162:165], v[18:25], v[34:41], v[162:165], v211, v211 op_sel_hi:[0,0,0]
	v_mfma_scale_f32_16x16x128_f8f6f4 v[158:161], v[26:33], v[34:41], v[158:161], v211, v211 op_sel_hi:[0,0,0]
	v_mfma_scale_f32_16x16x128_f8f6f4 v[154:157], v[18:25], v[42:49], v[154:157], v211, v211 op_sel_hi:[0,0,0]
	v_mfma_scale_f32_16x16x128_f8f6f4 v[150:153], v[26:33], v[42:49], v[150:153], v211, v211 op_sel_hi:[0,0,0]
	v_mfma_scale_f32_16x16x128_f8f6f4 v[146:149], v[18:25], v[50:57], v[146:149], v211, v211 op_sel_hi:[0,0,0]
	v_mfma_scale_f32_16x16x128_f8f6f4 v[142:145], v[26:33], v[50:57], v[142:145], v211, v211 op_sel_hi:[0,0,0]
	v_mfma_scale_f32_16x16x128_f8f6f4 v[138:141], v[18:25], v[58:65], v[138:141], v211, v211 op_sel_hi:[0,0,0]
	v_mfma_scale_f32_16x16x128_f8f6f4 v[134:137], v[26:33], v[58:65], v[134:137], v211, v211 op_sel_hi:[0,0,0]
	s_setprio 0
	s_barrier
	ds_read_b128 v[34:37], v213 offset:16384
	ds_read_b128 v[38:41], v213 offset:17408
	ds_read_b128 v[42:45], v213 offset:18432
	ds_read_b128 v[46:49], v213 offset:19456
	ds_read_b128 v[50:53], v213 offset:20480
	ds_read_b128 v[54:57], v213 offset:21504
	ds_read_b128 v[58:61], v213 offset:22528
	ds_read_b128 v[62:65], v213 offset:23552
	s_mov_b32 m0, s50
	s_nop 0
	global_load_lds_dwordx4 v198, s[30:31]
	s_nop 0
	s_mov_b32 m0, s51
	s_nop 0
	global_load_lds_dwordx4 v199, s[30:31]
	s_add_u32 s30, s8, 0x40100
	s_addc_u32 s31, s9, 0
	s_mov_b32 m0, s52
	s_nop 0
	global_load_lds_dwordx4 v198, s[30:31]
	s_nop 0
	s_mov_b32 m0, s53
	s_nop 0
	global_load_lds_dwordx4 v199, s[30:31]
	s_nop 0
	s_mov_b32 m0, s49
	s_nop 0
	global_load_lds_dwordx4 v202, s[12:13]
	s_nop 0
	s_mov_b32 m0, s55
	s_nop 0
	global_load_lds_dwordx4 v206, s[12:13]
	s_waitcnt vmcnt(24)
	s_waitcnt lgkmcnt(0)
	s_barrier
	s_setprio 1
	v_mfma_scale_f32_16x16x128_f8f6f4 v[130:133], v[2:9], v[34:41], v[130:133], v211, v211 op_sel_hi:[0,0,0]
	v_mfma_scale_f32_16x16x128_f8f6f4 v[126:129], v[10:17], v[34:41], v[126:129], v211, v211 op_sel_hi:[0,0,0]
	v_mfma_scale_f32_16x16x128_f8f6f4 v[122:125], v[2:9], v[42:49], v[122:125], v211, v211 op_sel_hi:[0,0,0]
	v_mfma_scale_f32_16x16x128_f8f6f4 v[118:121], v[10:17], v[42:49], v[118:121], v211, v211 op_sel_hi:[0,0,0]
	v_mfma_scale_f32_16x16x128_f8f6f4 v[114:117], v[2:9], v[50:57], v[114:117], v211, v211 op_sel_hi:[0,0,0]
	v_mfma_scale_f32_16x16x128_f8f6f4 v[110:113], v[10:17], v[50:57], v[110:113], v211, v211 op_sel_hi:[0,0,0]
	v_mfma_scale_f32_16x16x128_f8f6f4 v[106:109], v[2:9], v[58:65], v[106:109], v211, v211 op_sel_hi:[0,0,0]
	v_mfma_scale_f32_16x16x128_f8f6f4 v[102:105], v[10:17], v[58:65], v[102:105], v211, v211 op_sel_hi:[0,0,0]
	v_mfma_scale_f32_16x16x128_f8f6f4 v[98:101], v[18:25], v[34:41], v[98:101], v211, v211 op_sel_hi:[0,0,0]
	v_mfma_scale_f32_16x16x128_f8f6f4 v[94:97], v[26:33], v[34:41], v[94:97], v211, v211 op_sel_hi:[0,0,0]
	v_mfma_scale_f32_16x16x128_f8f6f4 v[90:93], v[18:25], v[42:49], v[90:93], v211, v211 op_sel_hi:[0,0,0]
	v_mfma_scale_f32_16x16x128_f8f6f4 v[86:89], v[26:33], v[42:49], v[86:89], v211, v211 op_sel_hi:[0,0,0]
	v_mfma_scale_f32_16x16x128_f8f6f4 v[82:85], v[18:25], v[50:57], v[82:85], v211, v211 op_sel_hi:[0,0,0]
	v_mfma_scale_f32_16x16x128_f8f6f4 v[78:81], v[26:33], v[50:57], v[78:81], v211, v211 op_sel_hi:[0,0,0]
	v_mfma_scale_f32_16x16x128_f8f6f4 v[74:77], v[18:25], v[58:65], v[74:77], v211, v211 op_sel_hi:[0,0,0]
	v_mfma_scale_f32_16x16x128_f8f6f4 v[70:73], v[26:33], v[58:65], v[70:73], v211, v211 op_sel_hi:[0,0,0]
	s_setprio 0
	s_barrier
	ds_read_b128 v[2:5], v69
	ds_read_b128 v[6:9], v69 offset:1024
	ds_read_b128 v[10:13], v69 offset:2048
	ds_read_b128 v[14:17], v69 offset:3072
	ds_read_b128 v[18:21], v215
	ds_read_b128 v[22:25], v215 offset:1024
	ds_read_b128 v[26:29], v215 offset:2048
	ds_read_b128 v[30:33], v215 offset:3072
	ds_read_b128 v[34:37], v213 offset:32768
	ds_read_b128 v[38:41], v213 offset:33792
	ds_read_b128 v[42:45], v213 offset:34816
	ds_read_b128 v[46:49], v213 offset:35840
	ds_read_b128 v[50:53], v213 offset:36864
	ds_read_b128 v[54:57], v213 offset:37888
	ds_read_b128 v[58:61], v213 offset:38912
	ds_read_b128 v[62:65], v213 offset:39936
	s_mov_b32 m0, s56
	s_nop 0
	global_load_lds_dwordx4 v204, s[12:13]
	s_nop 0
	s_mov_b32 m0, s57
	s_nop 0
	global_load_lds_dwordx4 v205, s[12:13]
	s_waitcnt vmcnt(8)
	s_waitcnt lgkmcnt(0)
	s_barrier
	s_setprio 1
	v_mfma_scale_f32_16x16x128_f8f6f4 v[194:197], v[2:9], v[34:41], v[194:197], v211, v211 op_sel_hi:[0,0,0]
	v_mfma_scale_f32_16x16x128_f8f6f4 v[190:193], v[10:17], v[34:41], v[190:193], v211, v211 op_sel_hi:[0,0,0]
	v_mfma_scale_f32_16x16x128_f8f6f4 v[186:189], v[2:9], v[42:49], v[186:189], v211, v211 op_sel_hi:[0,0,0]
	v_mfma_scale_f32_16x16x128_f8f6f4 v[182:185], v[10:17], v[42:49], v[182:185], v211, v211 op_sel_hi:[0,0,0]
	v_mfma_scale_f32_16x16x128_f8f6f4 v[178:181], v[2:9], v[50:57], v[178:181], v211, v211 op_sel_hi:[0,0,0]
	v_mfma_scale_f32_16x16x128_f8f6f4 v[174:177], v[10:17], v[50:57], v[174:177], v211, v211 op_sel_hi:[0,0,0]
	v_mfma_scale_f32_16x16x128_f8f6f4 v[170:173], v[2:9], v[58:65], v[170:173], v211, v211 op_sel_hi:[0,0,0]
	v_mfma_scale_f32_16x16x128_f8f6f4 v[166:169], v[10:17], v[58:65], v[166:169], v211, v211 op_sel_hi:[0,0,0]
	v_mfma_scale_f32_16x16x128_f8f6f4 v[162:165], v[18:25], v[34:41], v[162:165], v211, v211 op_sel_hi:[0,0,0]
	v_mfma_scale_f32_16x16x128_f8f6f4 v[158:161], v[26:33], v[34:41], v[158:161], v211, v211 op_sel_hi:[0,0,0]
	v_mfma_scale_f32_16x16x128_f8f6f4 v[154:157], v[18:25], v[42:49], v[154:157], v211, v211 op_sel_hi:[0,0,0]
	v_mfma_scale_f32_16x16x128_f8f6f4 v[150:153], v[26:33], v[42:49], v[150:153], v211, v211 op_sel_hi:[0,0,0]
	v_mfma_scale_f32_16x16x128_f8f6f4 v[146:149], v[18:25], v[50:57], v[146:149], v211, v211 op_sel_hi:[0,0,0]
	v_mfma_scale_f32_16x16x128_f8f6f4 v[142:145], v[26:33], v[50:57], v[142:145], v211, v211 op_sel_hi:[0,0,0]
	v_mfma_scale_f32_16x16x128_f8f6f4 v[138:141], v[18:25], v[58:65], v[138:141], v211, v211 op_sel_hi:[0,0,0]
	v_mfma_scale_f32_16x16x128_f8f6f4 v[134:137], v[26:33], v[58:65], v[134:137], v211, v211 op_sel_hi:[0,0,0]
	s_setprio 0
	s_barrier
	ds_read_b128 v[34:37], v213 offset:49152
	ds_read_b128 v[38:41], v213 offset:50176
	ds_read_b128 v[42:45], v213 offset:51200
	ds_read_b128 v[46:49], v213 offset:52224
	ds_read_b128 v[50:53], v213 offset:53248
	ds_read_b128 v[54:57], v213 offset:54272
	ds_read_b128 v[58:61], v213 offset:55296
	ds_read_b128 v[62:65], v213 offset:56320
	s_add_u32 s30, s8, 0x180
	s_addc_u32 s31, s9, 0
	s_mov_b32 m0, s58
	s_nop 0
	global_load_lds_dwordx4 v198, s[30:31]
	s_nop 0
	s_mov_b32 m0, s59
	s_nop 0
	global_load_lds_dwordx4 v199, s[30:31]
	s_add_u32 s30, s8, 0x40180
	s_addc_u32 s31, s9, 0
	s_mov_b32 m0, s62
	s_nop 0
	global_load_lds_dwordx4 v198, s[30:31]
	s_nop 0
	s_mov_b32 m0, s63
	s_nop 0
	global_load_lds_dwordx4 v199, s[30:31]
	s_nop 0
	s_mov_b32 m0, s60
	s_nop 0
	global_load_lds_dwordx4 v202, s[14:15]
	s_nop 0
	s_mov_b32 m0, s61
	s_nop 0
	global_load_lds_dwordx4 v206, s[14:15]
	s_waitcnt vmcnt(8)
	s_waitcnt lgkmcnt(0)
	s_barrier
	s_setprio 1
	v_mfma_scale_f32_16x16x128_f8f6f4 v[130:133], v[2:9], v[34:41], v[130:133], v211, v211 op_sel_hi:[0,0,0]
	v_mfma_scale_f32_16x16x128_f8f6f4 v[126:129], v[10:17], v[34:41], v[126:129], v211, v211 op_sel_hi:[0,0,0]
	v_mfma_scale_f32_16x16x128_f8f6f4 v[122:125], v[2:9], v[42:49], v[122:125], v211, v211 op_sel_hi:[0,0,0]
	v_mfma_scale_f32_16x16x128_f8f6f4 v[118:121], v[10:17], v[42:49], v[118:121], v211, v211 op_sel_hi:[0,0,0]
	v_mfma_scale_f32_16x16x128_f8f6f4 v[114:117], v[2:9], v[50:57], v[114:117], v211, v211 op_sel_hi:[0,0,0]
	v_mfma_scale_f32_16x16x128_f8f6f4 v[110:113], v[10:17], v[50:57], v[110:113], v211, v211 op_sel_hi:[0,0,0]
	v_mfma_scale_f32_16x16x128_f8f6f4 v[106:109], v[2:9], v[58:65], v[106:109], v211, v211 op_sel_hi:[0,0,0]
	v_mfma_scale_f32_16x16x128_f8f6f4 v[102:105], v[10:17], v[58:65], v[102:105], v211, v211 op_sel_hi:[0,0,0]
	v_mfma_scale_f32_16x16x128_f8f6f4 v[98:101], v[18:25], v[34:41], v[98:101], v211, v211 op_sel_hi:[0,0,0]
	v_mfma_scale_f32_16x16x128_f8f6f4 v[94:97], v[26:33], v[34:41], v[94:97], v211, v211 op_sel_hi:[0,0,0]
	v_mfma_scale_f32_16x16x128_f8f6f4 v[90:93], v[18:25], v[42:49], v[90:93], v211, v211 op_sel_hi:[0,0,0]
	v_mfma_scale_f32_16x16x128_f8f6f4 v[86:89], v[26:33], v[42:49], v[86:89], v211, v211 op_sel_hi:[0,0,0]
	v_mfma_scale_f32_16x16x128_f8f6f4 v[82:85], v[18:25], v[50:57], v[82:85], v211, v211 op_sel_hi:[0,0,0]
	v_mfma_scale_f32_16x16x128_f8f6f4 v[78:81], v[26:33], v[50:57], v[78:81], v211, v211 op_sel_hi:[0,0,0]
	v_mfma_scale_f32_16x16x128_f8f6f4 v[74:77], v[18:25], v[58:65], v[74:77], v211, v211 op_sel_hi:[0,0,0]
	v_mfma_scale_f32_16x16x128_f8f6f4 v[70:73], v[26:33], v[58:65], v[70:73], v211, v211 op_sel_hi:[0,0,0]
	s_setprio 0
	s_barrier
	s_mov_b32 s34, 2
	s_branch .LBB0_2902

.LBB0_2903:
	s_add_i32 s44, s42, 0xdc600100
	s_and_b64 s[42:43], s[38:39], exec
	s_cselect_b32 s77, s44, 0
	s_add_u32 s42, s41, s40
	s_addc_u32 s43, s76, 0
	s_waitcnt vmcnt(8)
	s_and_b64 s[38:39], s[38:39], exec
	s_waitcnt lgkmcnt(0)
	s_cselect_b32 s38, s42, s29
	s_cselect_b32 s39, s43, s2
	s_add_u32 s42, s38, 0x80
	s_addc_u32 s43, s39, 0
	s_barrier
	s_setprio 1
	v_mfma_scale_f32_16x16x128_f8f6f4 v[194:197], v[18:25], v[58:65], v[194:197], v211, v211 op_sel_hi:[0,0,0]
	v_mfma_scale_f32_16x16x128_f8f6f4 v[190:193], v[26:33], v[58:65], v[190:193], v211, v211 op_sel_hi:[0,0,0]
	v_mfma_scale_f32_16x16x128_f8f6f4 v[186:189], v[18:25], v[50:57], v[186:189], v211, v211 op_sel_hi:[0,0,0]
	v_mfma_scale_f32_16x16x128_f8f6f4 v[182:185], v[26:33], v[50:57], v[182:185], v211, v211 op_sel_hi:[0,0,0]
	v_mfma_scale_f32_16x16x128_f8f6f4 v[178:181], v[18:25], v[42:49], v[178:181], v211, v211 op_sel_hi:[0,0,0]
	v_mfma_scale_f32_16x16x128_f8f6f4 v[174:177], v[26:33], v[42:49], v[174:177], v211, v211 op_sel_hi:[0,0,0]
	v_mfma_scale_f32_16x16x128_f8f6f4 v[170:173], v[18:25], v[34:41], v[170:173], v211, v211 op_sel_hi:[0,0,0]
	v_mfma_scale_f32_16x16x128_f8f6f4 v[166:169], v[26:33], v[34:41], v[166:169], v211, v211 op_sel_hi:[0,0,0]
	v_mfma_scale_f32_16x16x128_f8f6f4 v[162:165], v[2:9], v[58:65], v[162:165], v211, v211 op_sel_hi:[0,0,0]
	v_mfma_scale_f32_16x16x128_f8f6f4 v[158:161], v[10:17], v[58:65], v[158:161], v211, v211 op_sel_hi:[0,0,0]
	v_mfma_scale_f32_16x16x128_f8f6f4 v[154:157], v[2:9], v[50:57], v[154:157], v211, v211 op_sel_hi:[0,0,0]
	v_mfma_scale_f32_16x16x128_f8f6f4 v[150:153], v[10:17], v[50:57], v[150:153], v211, v211 op_sel_hi:[0,0,0]
	v_mfma_scale_f32_16x16x128_f8f6f4 v[146:149], v[2:9], v[42:49], v[146:149], v211, v211 op_sel_hi:[0,0,0]
	v_mfma_scale_f32_16x16x128_f8f6f4 v[142:145], v[10:17], v[42:49], v[142:145], v211, v211 op_sel_hi:[0,0,0]
	v_mfma_scale_f32_16x16x128_f8f6f4 v[138:141], v[2:9], v[34:41], v[138:141], v211, v211 op_sel_hi:[0,0,0]
	v_mfma_scale_f32_16x16x128_f8f6f4 v[134:137], v[10:17], v[34:41], v[134:137], v211, v211 op_sel_hi:[0,0,0]
	s_setprio 0
	s_barrier
	ds_read_b128 v[34:37], v213 offset:16384
	ds_read_b128 v[38:41], v213 offset:17408
	ds_read_b128 v[42:45], v213 offset:18432
	ds_read_b128 v[46:49], v213 offset:19456
	ds_read_b128 v[50:53], v213 offset:20480
	ds_read_b128 v[54:57], v213 offset:21504
	ds_read_b128 v[58:61], v213 offset:22528
	ds_read_b128 v[62:65], v213 offset:23552
	s_mov_b32 m0, s50
	s_nop 0
	global_load_lds_dwordx4 v198, s[38:39]
	s_add_u32 s44, s38, 0x40000
	s_mov_b32 m0, s51
	s_nop 0
	global_load_lds_dwordx4 v199, s[38:39]
	s_addc_u32 s45, s39, 0
	s_mov_b32 m0, s52
	s_nop 0
	global_load_lds_dwordx4 v198, s[44:45]
	s_nop 0
	s_mov_b32 m0, s53
	s_nop 0
	global_load_lds_dwordx4 v199, s[44:45]
	s_add_u32 s44, s6, s77
	s_addc_u32 s45, s7, 0
	s_mov_b32 m0, s49
	s_nop 0
	global_load_lds_dwordx4 v202, s[44:45]
	s_nop 0
	s_mov_b32 m0, s55
	s_nop 0
	global_load_lds_dwordx4 v206, s[44:45]
	s_waitcnt vmcnt(8)
	s_waitcnt lgkmcnt(0)
	s_barrier
	s_setprio 1
	v_mfma_scale_f32_16x16x128_f8f6f4 v[130:133], v[18:25], v[34:41], v[130:133], v211, v211 op_sel_hi:[0,0,0]
	v_mfma_scale_f32_16x16x128_f8f6f4 v[126:129], v[26:33], v[34:41], v[126:129], v211, v211 op_sel_hi:[0,0,0]
	v_mfma_scale_f32_16x16x128_f8f6f4 v[122:125], v[18:25], v[42:49], v[122:125], v211, v211 op_sel_hi:[0,0,0]
	v_mfma_scale_f32_16x16x128_f8f6f4 v[118:121], v[26:33], v[42:49], v[118:121], v211, v211 op_sel_hi:[0,0,0]
	v_mfma_scale_f32_16x16x128_f8f6f4 v[114:117], v[18:25], v[50:57], v[114:117], v211, v211 op_sel_hi:[0,0,0]
	v_mfma_scale_f32_16x16x128_f8f6f4 v[110:113], v[26:33], v[50:57], v[110:113], v211, v211 op_sel_hi:[0,0,0]
	v_mfma_scale_f32_16x16x128_f8f6f4 v[106:109], v[18:25], v[58:65], v[106:109], v211, v211 op_sel_hi:[0,0,0]
	v_mfma_scale_f32_16x16x128_f8f6f4 v[102:105], v[26:33], v[58:65], v[102:105], v211, v211 op_sel_hi:[0,0,0]
	v_mfma_scale_f32_16x16x128_f8f6f4 v[98:101], v[2:9], v[34:41], v[98:101], v211, v211 op_sel_hi:[0,0,0]
	v_mfma_scale_f32_16x16x128_f8f6f4 v[94:97], v[10:17], v[34:41], v[94:97], v211, v211 op_sel_hi:[0,0,0]
	v_mfma_scale_f32_16x16x128_f8f6f4 v[90:93], v[2:9], v[42:49], v[90:93], v211, v211 op_sel_hi:[0,0,0]
	v_mfma_scale_f32_16x16x128_f8f6f4 v[86:89], v[10:17], v[42:49], v[86:89], v211, v211 op_sel_hi:[0,0,0]
	v_mfma_scale_f32_16x16x128_f8f6f4 v[82:85], v[2:9], v[50:57], v[82:85], v211, v211 op_sel_hi:[0,0,0]
	v_mfma_scale_f32_16x16x128_f8f6f4 v[78:81], v[10:17], v[50:57], v[78:81], v211, v211 op_sel_hi:[0,0,0]
	v_mfma_scale_f32_16x16x128_f8f6f4 v[74:77], v[2:9], v[58:65], v[74:77], v211, v211 op_sel_hi:[0,0,0]
	v_mfma_scale_f32_16x16x128_f8f6f4 v[70:73], v[10:17], v[58:65], v[70:73], v211, v211 op_sel_hi:[0,0,0]
	s_setprio 0
	s_barrier
	ds_read_b128 v[2:5], v69
	ds_read_b128 v[6:9], v69 offset:1024
	ds_read_b128 v[10:13], v69 offset:2048
	ds_read_b128 v[14:17], v69 offset:3072
	ds_read_b128 v[18:21], v215
	ds_read_b128 v[22:25], v215 offset:1024
	ds_read_b128 v[26:29], v215 offset:2048
	ds_read_b128 v[30:33], v215 offset:3072
	ds_read_b128 v[34:37], v213 offset:32768
	ds_read_b128 v[38:41], v213 offset:33792
	ds_read_b128 v[42:45], v213 offset:34816
	ds_read_b128 v[46:49], v213 offset:35840
	ds_read_b128 v[50:53], v213 offset:36864
	ds_read_b128 v[54:57], v213 offset:37888
	ds_read_b128 v[58:61], v213 offset:38912
	ds_read_b128 v[62:65], v213 offset:39936
	s_mov_b32 m0, s56
	s_nop 0
	global_load_lds_dwordx4 v204, s[44:45]
	s_nop 0
	s_mov_b32 m0, s57
	s_nop 0
	global_load_lds_dwordx4 v205, s[44:45]
	s_waitcnt vmcnt(8)
	s_waitcnt lgkmcnt(0)
	s_barrier
	s_setprio 1
	v_mfma_scale_f32_16x16x128_f8f6f4 v[194:197], v[2:9], v[34:41], v[194:197], v211, v211 op_sel_hi:[0,0,0]
	v_mfma_scale_f32_16x16x128_f8f6f4 v[190:193], v[10:17], v[34:41], v[190:193], v211, v211 op_sel_hi:[0,0,0]
	v_mfma_scale_f32_16x16x128_f8f6f4 v[186:189], v[2:9], v[42:49], v[186:189], v211, v211 op_sel_hi:[0,0,0]
	v_mfma_scale_f32_16x16x128_f8f6f4 v[182:185], v[10:17], v[42:49], v[182:185], v211, v211 op_sel_hi:[0,0,0]
	v_mfma_scale_f32_16x16x128_f8f6f4 v[178:181], v[2:9], v[50:57], v[178:181], v211, v211 op_sel_hi:[0,0,0]
	v_mfma_scale_f32_16x16x128_f8f6f4 v[174:177], v[10:17], v[50:57], v[174:177], v211, v211 op_sel_hi:[0,0,0]
	v_mfma_scale_f32_16x16x128_f8f6f4 v[170:173], v[2:9], v[58:65], v[170:173], v211, v211 op_sel_hi:[0,0,0]
	v_mfma_scale_f32_16x16x128_f8f6f4 v[166:169], v[10:17], v[58:65], v[166:169], v211, v211 op_sel_hi:[0,0,0]
	v_mfma_scale_f32_16x16x128_f8f6f4 v[162:165], v[18:25], v[34:41], v[162:165], v211, v211 op_sel_hi:[0,0,0]
	v_mfma_scale_f32_16x16x128_f8f6f4 v[158:161], v[26:33], v[34:41], v[158:161], v211, v211 op_sel_hi:[0,0,0]
	v_mfma_scale_f32_16x16x128_f8f6f4 v[154:157], v[18:25], v[42:49], v[154:157], v211, v211 op_sel_hi:[0,0,0]
	v_mfma_scale_f32_16x16x128_f8f6f4 v[150:153], v[26:33], v[42:49], v[150:153], v211, v211 op_sel_hi:[0,0,0]
	v_mfma_scale_f32_16x16x128_f8f6f4 v[146:149], v[18:25], v[50:57], v[146:149], v211, v211 op_sel_hi:[0,0,0]
	v_mfma_scale_f32_16x16x128_f8f6f4 v[142:145], v[26:33], v[50:57], v[142:145], v211, v211 op_sel_hi:[0,0,0]
	v_mfma_scale_f32_16x16x128_f8f6f4 v[138:141], v[18:25], v[58:65], v[138:141], v211, v211 op_sel_hi:[0,0,0]
	v_mfma_scale_f32_16x16x128_f8f6f4 v[134:137], v[26:33], v[58:65], v[134:137], v211, v211 op_sel_hi:[0,0,0]
	s_setprio 0
	s_barrier
	ds_read_b128 v[34:37], v213 offset:49152
	ds_read_b128 v[38:41], v213 offset:50176
	ds_read_b128 v[42:45], v213 offset:51200
	ds_read_b128 v[46:49], v213 offset:52224
	ds_read_b128 v[50:53], v213 offset:53248
	ds_read_b128 v[54:57], v213 offset:54272
	ds_read_b128 v[58:61], v213 offset:55296
	ds_read_b128 v[62:65], v213 offset:56320
	s_mov_b32 m0, s58
	s_nop 0
	global_load_lds_dwordx4 v198, s[42:43]
	s_add_u32 s38, s38, 0x40080
	s_mov_b32 m0, s59
	s_nop 0
	global_load_lds_dwordx4 v199, s[42:43]
	s_addc_u32 s39, s39, 0
	s_mov_b32 m0, s62
	s_nop 0
	global_load_lds_dwordx4 v198, s[38:39]
	s_nop 0
	s_mov_b32 m0, s63
	s_nop 0
	global_load_lds_dwordx4 v199, s[38:39]
	s_add_u32 s38, s44, 0x80
	s_addc_u32 s39, s45, 0
	s_mov_b32 m0, s60
	s_nop 0
	global_load_lds_dwordx4 v202, s[38:39]
	s_nop 0
	s_mov_b32 m0, s61
	s_nop 0
	global_load_lds_dwordx4 v206, s[38:39]
	s_waitcnt vmcnt(8)
	s_waitcnt lgkmcnt(0)
	s_barrier
	s_setprio 1
	v_mfma_scale_f32_16x16x128_f8f6f4 v[130:133], v[2:9], v[34:41], v[130:133], v211, v211 op_sel_hi:[0,0,0]
	v_mfma_scale_f32_16x16x128_f8f6f4 v[126:129], v[10:17], v[34:41], v[126:129], v211, v211 op_sel_hi:[0,0,0]
	v_mfma_scale_f32_16x16x128_f8f6f4 v[122:125], v[2:9], v[42:49], v[122:125], v211, v211 op_sel_hi:[0,0,0]
	v_mfma_scale_f32_16x16x128_f8f6f4 v[118:121], v[10:17], v[42:49], v[118:121], v211, v211 op_sel_hi:[0,0,0]
	v_mfma_scale_f32_16x16x128_f8f6f4 v[114:117], v[2:9], v[50:57], v[114:117], v211, v211 op_sel_hi:[0,0,0]
	v_mfma_scale_f32_16x16x128_f8f6f4 v[110:113], v[10:17], v[50:57], v[110:113], v211, v211 op_sel_hi:[0,0,0]
	v_mfma_scale_f32_16x16x128_f8f6f4 v[106:109], v[2:9], v[58:65], v[106:109], v211, v211 op_sel_hi:[0,0,0]
	v_mfma_scale_f32_16x16x128_f8f6f4 v[102:105], v[10:17], v[58:65], v[102:105], v211, v211 op_sel_hi:[0,0,0]
	v_mfma_scale_f32_16x16x128_f8f6f4 v[98:101], v[18:25], v[34:41], v[98:101], v211, v211 op_sel_hi:[0,0,0]
	v_mfma_scale_f32_16x16x128_f8f6f4 v[94:97], v[26:33], v[34:41], v[94:97], v211, v211 op_sel_hi:[0,0,0]
	v_mfma_scale_f32_16x16x128_f8f6f4 v[90:93], v[18:25], v[42:49], v[90:93], v211, v211 op_sel_hi:[0,0,0]
	v_mfma_scale_f32_16x16x128_f8f6f4 v[86:89], v[26:33], v[42:49], v[86:89], v211, v211 op_sel_hi:[0,0,0]
	v_mfma_scale_f32_16x16x128_f8f6f4 v[82:85], v[18:25], v[50:57], v[82:85], v211, v211 op_sel_hi:[0,0,0]
	v_mfma_scale_f32_16x16x128_f8f6f4 v[78:81], v[26:33], v[50:57], v[78:81], v211, v211 op_sel_hi:[0,0,0]
	v_mfma_scale_f32_16x16x128_f8f6f4 v[74:77], v[18:25], v[58:65], v[74:77], v211, v211 op_sel_hi:[0,0,0]
	v_mfma_scale_f32_16x16x128_f8f6f4 v[70:73], v[26:33], v[58:65], v[70:73], v211, v211 op_sel_hi:[0,0,0]
	s_setprio 0
	s_barrier
	s_add_i32 s33, s33, 2
	s_add_u32 s41, s41, 0x100
	s_addc_u32 s76, s76, 0
	s_add_u32 s36, s36, 0x100
	s_addc_u32 s37, s37, 0
	s_add_u32 s34, s34, 0x100
	s_addc_u32 s35, s35, 0
	s_cmp_gt_u32 s33, 13
	s_cbranch_scc1 .LBB0_2906
